# peer_gather row loads in SGPR-base form (table base + id*512 on the SALU), attention softplus log simplified, DPP reductions in attention epilogue
# speedup vs baseline: 1.0152x; 1.0094x over previous
.LBB0_253:
	s_ashr_i32 s6, s15, 7
	s_lshl_b32 s7, s15, 5
	s_and_b32 s22, s7, 0xfe0
	s_ashr_i32 s7, s6, 31
	s_lshl_b64 s[10:11], s[6:7], 12
	s_or_b32 s20, s10, s22
	v_or_b32_e32 v0, s20, v64
	v_mad_u64_u32 v[4:5], s[6:7], v0, s27, v[100:101]
	v_mad_i32_i24 v5, s11, v192, v5
	v_or_b32_e32 v110, s20, v66
	global_load_dwordx4 v[48:51], v[4:5], off offset:1024
	global_load_dwordx4 v[52:55], v[4:5], off offset:1056
	global_load_dwordx4 v[56:59], v[4:5], off offset:1088
	global_load_dwordx4 v[60:63], v[4:5], off offset:1120
	global_load_dwordx4 v[0:3], v[4:5], off offset:2048
	global_load_dwordx4 v[112:115], v[4:5], off offset:2080
	global_load_dwordx4 v[116:119], v[4:5], off offset:2112
	global_load_dwordx4 v[120:123], v[4:5], off offset:2144
	v_mad_u64_u32 v[4:5], s[6:7], v110, s27, v[102:103]
	v_mad_i32_i24 v5, s11, v192, v5
	v_add_co_u32_e32 v6, vcc, s26, v4
	s_movk_i32 s6, 0x3000
	s_nop 0
	v_addc_co_u32_e32 v7, vcc, 0, v5, vcc
	v_add_co_u32_e32 v8, vcc, s6, v4
	s_mov_b32 s6, 0x9000
	s_nop 0
	v_addc_co_u32_e32 v9, vcc, 0, v5, vcc
	v_add_co_u32_e32 v10, vcc, s87, v4
	s_mov_b32 s21, s11
	s_nop 0
	v_addc_co_u32_e32 v11, vcc, 0, v5, vcc
	v_add_co_u32_e32 v12, vcc, s6, v4
	s_mov_b32 s6, 0xa000
	s_nop 0
	v_addc_co_u32_e32 v13, vcc, 0, v5, vcc
	global_load_ushort v19, v[6:7], off offset:3584
	global_load_ushort v16, v[6:7], off offset:3648
	global_load_ushort v21, v[8:9], off
	global_load_ushort v17, v[8:9], off offset:64
	global_load_ushort v22, v[10:11], off offset:512
	global_load_ushort v18, v[10:11], off offset:576
	global_load_ushort v23, v[12:13], off offset:3072
	global_load_ushort v20, v[12:13], off offset:3136
	v_add_co_u32_e32 v6, vcc, s6, v4
	s_mov_b32 s6, 0xc000
	s_nop 0
	v_addc_co_u32_e32 v7, vcc, 0, v5, vcc
	v_add_co_u32_e32 v8, vcc, s6, v4
	s_mov_b32 s6, 0xd000
	s_nop 0
	v_addc_co_u32_e32 v9, vcc, 0, v5, vcc
	v_add_co_u32_e32 v10, vcc, s6, v4
	s_mov_b32 s6, 0x12000
	s_nop 0
	v_addc_co_u32_e32 v11, vcc, 0, v5, vcc
	v_add_co_u32_e32 v12, vcc, s6, v4
	s_mov_b32 s6, 0x13000
	s_nop 0
	v_addc_co_u32_e32 v13, vcc, 0, v5, vcc
	global_load_ushort v27, v[6:7], off offset:3584
	global_load_ushort v24, v[6:7], off offset:3648
	global_load_ushort v28, v[8:9], off
	global_load_ushort v25, v[8:9], off offset:64
	global_load_ushort v29, v[10:11], off offset:512
	global_load_ushort v26, v[10:11], off offset:576
	global_load_ushort v33, v[12:13], off offset:3072
	global_load_ushort v32, v[12:13], off offset:3136
	v_add_co_u32_e32 v6, vcc, s6, v4
	s_mov_b32 s6, 0x15000
	s_nop 0
	v_addc_co_u32_e32 v7, vcc, 0, v5, vcc
	v_add_co_u32_e32 v8, vcc, s6, v4
	s_mov_b32 s6, 0x16000
	s_nop 0
	v_addc_co_u32_e32 v9, vcc, 0, v5, vcc
	v_add_co_u32_e32 v10, vcc, s6, v4
	s_mov_b32 s6, 0x1b000
	s_nop 0
	v_addc_co_u32_e32 v11, vcc, 0, v5, vcc
	v_add_co_u32_e32 v12, vcc, s6, v4
	s_mov_b32 s6, 0x1c000
	s_nop 0
	v_addc_co_u32_e32 v13, vcc, 0, v5, vcc
	global_load_ushort v37, v[6:7], off offset:3584
	global_load_ushort v34, v[6:7], off offset:3648
	global_load_ushort v39, v[8:9], off
	global_load_ushort v35, v[8:9], off offset:64
	global_load_ushort v40, v[10:11], off offset:512
	global_load_ushort v36, v[10:11], off offset:576
	global_load_ushort v41, v[12:13], off offset:3072
	global_load_ushort v38, v[12:13], off offset:3136
	v_add_co_u32_e32 v6, vcc, s6, v4
	s_mov_b32 s6, 0x1e000
	s_nop 0
	v_addc_co_u32_e32 v7, vcc, 0, v5, vcc
	v_add_co_u32_e32 v8, vcc, s6, v4
	s_mov_b32 s6, 0x1f000
	s_nop 0
	v_addc_co_u32_e32 v9, vcc, 0, v5, vcc
	v_add_co_u32_e32 v10, vcc, s6, v4
	v_mov_b32_e32 v111, s11
	s_nop 0
	v_addc_co_u32_e32 v11, vcc, 0, v5, vcc
	global_load_ushort v31, v[4:5], off offset:3072
	global_load_ushort v30, v[4:5], off offset:3136
	global_load_ushort v45, v[6:7], off offset:3584
	global_load_ushort v42, v[6:7], off offset:3648
	global_load_ushort v46, v[8:9], off
	global_load_ushort v43, v[8:9], off offset:64
	global_load_ushort v47, v[10:11], off offset:512
	global_load_ushort v44, v[10:11], off offset:576
	s_nop 15
	s_nop 15
	s_waitcnt vmcnt(35)
	v_mfma_f32_32x32x16_bf16 v[0:15], v[0:3], v[48:51], 0
	s_waitcnt vmcnt(34)
	v_mfma_f32_32x32x16_bf16 v[0:15], v[112:115], v[52:55], v[0:15]
	s_waitcnt vmcnt(33)
	v_mfma_f32_32x32x16_bf16 v[0:15], v[116:119], v[56:59], v[0:15]
	s_waitcnt vmcnt(32)
	v_mfma_f32_32x32x16_bf16 v[0:15], v[120:123], v[60:63], v[0:15]
	s_nop 15
	s_nop 15
	s_nop 11
	v_mul_f32_e32 v0, 0x3e000000, v0
	v_mul_f32_e64 v79, |v0|, s28
	v_exp_f32_e32 v79, v79
	v_mul_f32_e32 v1, 0x3e000000, v1
	v_mul_f32_e64 v83, |v1|, s28
	v_exp_f32_e32 v83, v83
	v_add_f32_e32 v79, 1.0, v79
	v_mul_f32_e32 v2, 0x3e000000, v2
	v_mul_f32_e32 v3, 0x3e000000, v3
	v_log_f32_e32 v79, v79
	v_max_f32_e32 v81, 0, v0
	v_min_f32_e32 v0, 0, v0
	v_mul_f32_e32 v87, 0x3f317217, v79
	v_fma_f32 v87, v79, s30, -v87
	v_fmac_f32_e32 v87, 0x3377d1cf, v79
	s_nop 1
	v_fma_f32 v79, v79, s30, v87
	v_add_f32_e32 v81, v81, v79
	v_sub_f32_e32 v0, v0, v79
	v_add_f32_e32 v79, 1.0, v83
	v_cndmask_b32_e64 v81, 0, -v81, s[48:49]
	s_nop 0
	v_log_f32_e32 v79, v79
	v_cndmask_b32_e64 v83, v194, v0, s[48:49]
	v_max_f32_e32 v0, 0, v1
	v_min_f32_e32 v1, 0, v1
	v_mul_f32_e32 v85, 0x3f317217, v79
	v_fma_f32 v85, v79, s30, -v85
	v_fmac_f32_e32 v85, 0x3377d1cf, v79
	s_nop 1
	v_fma_f32 v79, v79, s30, v85
	v_mul_f32_e64 v85, |v2|, s28
	v_exp_f32_e32 v85, v85
	v_add_f32_e32 v0, v0, v79
	v_sub_f32_e32 v1, v1, v79
	v_cndmask_b32_e64 v87, 0, -v0, s[50:51]
	v_add_f32_e32 v79, 1.0, v85
	v_max_f32_e32 v0, 0, v2
	v_min_f32_e32 v2, 0, v2
	v_log_f32_e32 v79, v79
	v_cndmask_b32_e64 v85, v194, v1, s[50:51]
	v_mul_f32_e32 v1, 0x3f317217, v79
	v_fma_f32 v1, v79, s30, -v1
	v_fmac_f32_e32 v1, 0x3377d1cf, v79
	s_nop 1
	v_fma_f32 v1, v79, s30, v1
	v_mul_f32_e64 v79, |v3|, s28
	v_exp_f32_e32 v79, v79
	v_add_f32_e32 v0, v0, v1
	v_sub_f32_e32 v1, v2, v1
	v_cndmask_b32_e64 v89, 0, -v0, s[52:53]
	v_add_f32_e32 v2, 1.0, v79
	v_max_f32_e32 v0, 0, v3
	v_min_f32_e32 v3, 0, v3
	v_log_f32_e32 v2, v2
	v_cndmask_b32_e64 v79, v194, v1, s[52:53]
	v_mul_f32_e32 v1, 0x3f317217, v2
	v_fma_f32 v1, v2, s30, -v1
	v_fmac_f32_e32 v1, 0x3377d1cf, v2
	s_nop 1
	v_fma_f32 v1, v2, s30, v1
	v_mul_f32_e32 v2, 0x3e000000, v4
	v_mul_f32_e64 v4, |v2|, s28
	v_exp_f32_e32 v4, v4
	v_add_f32_e32 v0, v0, v1
	v_sub_f32_e32 v1, v3, v1
	v_cndmask_b32_e64 v91, v194, v1, s[54:55]
	v_add_f32_e32 v3, 1.0, v4
	v_cndmask_b32_e64 v93, 0, -v0, s[54:55]
	v_max_f32_e32 v0, 0, v2
	v_log_f32_e32 v3, v3
	v_min_f32_e32 v2, 0, v2
	v_mul_f32_e32 v1, 0x3f317217, v3
	v_fma_f32 v1, v3, s30, -v1
	v_fmac_f32_e32 v1, 0x3377d1cf, v3
	s_nop 1
	v_fma_f32 v1, v3, s30, v1
	v_mul_f32_e32 v3, 0x3e000000, v5
	v_mul_f32_e64 v4, |v3|, s28
	v_exp_f32_e32 v4, v4
	v_add_f32_e32 v0, v0, v1
	v_sub_f32_e32 v1, v2, v1
	v_cndmask_b32_e64 v95, v194, v1, s[56:57]
	v_add_f32_e32 v2, 1.0, v4
	v_cndmask_b32_e64 v5, 0, -v0, s[56:57]
	v_max_f32_e32 v0, 0, v3
	v_log_f32_e32 v2, v2
	v_min_f32_e32 v3, 0, v3
	v_mul_f32_e32 v1, 0x3f317217, v2
	v_fma_f32 v1, v2, s30, -v1
	v_fmac_f32_e32 v1, 0x3377d1cf, v2
	s_nop 1
	v_fma_f32 v1, v2, s30, v1
	v_mul_f32_e32 v2, 0x3e000000, v6
	v_mul_f32_e64 v4, |v2|, s28
	v_exp_f32_e32 v4, v4
	v_add_f32_e32 v0, v0, v1
	v_sub_f32_e32 v1, v3, v1
	v_cndmask_b32_e64 v97, v194, v1, s[58:59]
	v_add_f32_e32 v3, 1.0, v4
	v_cndmask_b32_e64 v112, 0, -v0, s[58:59]
	v_max_f32_e32 v0, 0, v2
	v_log_f32_e32 v3, v3
	v_min_f32_e32 v2, 0, v2
	v_mul_f32_e32 v1, 0x3f317217, v3
	v_fma_f32 v1, v3, s30, -v1
	v_fmac_f32_e32 v1, 0x3377d1cf, v3
	s_nop 1
	v_fma_f32 v1, v3, s30, v1
	v_mul_f32_e32 v3, 0x3e000000, v7
	v_mul_f32_e64 v4, |v3|, s28
	v_exp_f32_e32 v4, v4
	v_add_f32_e32 v0, v0, v1
	v_sub_f32_e32 v1, v2, v1
	v_cndmask_b32_e64 v113, v194, v1, s[60:61]
	v_add_f32_e32 v2, 1.0, v4
	v_cndmask_b32_e64 v114, 0, -v0, s[60:61]
	v_max_f32_e32 v0, 0, v3
	v_log_f32_e32 v2, v2
	v_min_f32_e32 v3, 0, v3
	v_mul_f32_e32 v1, 0x3f317217, v2
	v_fma_f32 v1, v2, s30, -v1
	v_fmac_f32_e32 v1, 0x3377d1cf, v2
	s_nop 1
	v_fma_f32 v1, v2, s30, v1
	v_mul_f32_e32 v2, 0x3e000000, v8
	v_mul_f32_e64 v4, |v2|, s28
	v_exp_f32_e32 v4, v4
	v_add_f32_e32 v0, v0, v1
	v_sub_f32_e32 v1, v3, v1
	v_cndmask_b32_e64 v115, v194, v1, s[62:63]
	v_add_f32_e32 v3, 1.0, v4
	v_cndmask_b32_e64 v116, 0, -v0, s[62:63]
	v_max_f32_e32 v0, 0, v2
	v_log_f32_e32 v3, v3
	v_min_f32_e32 v2, 0, v2
	v_mul_f32_e32 v1, 0x3f317217, v3
	v_fma_f32 v1, v3, s30, -v1
	v_fmac_f32_e32 v1, 0x3377d1cf, v3
	s_nop 1
	v_fma_f32 v1, v3, s30, v1
	v_mul_f32_e32 v3, 0x3e000000, v9
	v_mul_f32_e64 v4, |v3|, s28
	v_exp_f32_e32 v4, v4
	v_add_f32_e32 v0, v0, v1
	v_sub_f32_e32 v1, v2, v1
	v_cndmask_b32_e64 v117, v194, v1, s[64:65]
	v_add_f32_e32 v2, 1.0, v4
	v_cmp_gt_f32_e32 vcc, s29, v2
	s_nop 1
	v_cndmask_b32_e64 v4, 0, 32, vcc
	v_ldexp_f32 v2, v2, v4
	v_log_f32_e32 v4, v2
	v_cndmask_b32_e64 v2, 0, -v0, s[64:65]
	v_max_f32_e32 v0, 0, v3
	v_min_f32_e32 v3, 0, v3
	v_mul_f32_e32 v1, 0x3f317217, v4
	v_fma_f32 v1, v4, s30, -v1
	v_fmac_f32_e32 v1, 0x3377d1cf, v4
	v_fmac_f32_e32 v1, 0x3f317217, v4
	v_cmp_lt_f32_e64 s[6:7], |v4|, s31
	s_nop 1
	v_cndmask_b32_e64 v1, v4, v1, s[6:7]
	v_cndmask_b32_e32 v4, 0, v193, vcc
	v_sub_f32_e32 v1, v1, v4
	v_mul_f32_e32 v4, 0x3e000000, v10
	v_mul_f32_e64 v6, |v4|, s28
	v_exp_f32_e32 v6, v6
	v_add_f32_e32 v0, v0, v1
	v_sub_f32_e32 v1, v3, v1
	v_cndmask_b32_e64 v118, v194, v1, s[66:67]
	v_add_f32_e32 v3, 1.0, v6
	v_max_f32_e32 v1, 0, v4
	v_min_f32_e32 v4, 0, v4
	v_log_f32_e32 v3, v3
	v_cndmask_b32_e64 v0, 0, -v0, s[66:67]
	v_mul_f32_e32 v6, 0x3f317217, v3
	v_fma_f32 v6, v3, s30, -v6
	v_fmac_f32_e32 v6, 0x3377d1cf, v3
	s_nop 1
	v_fma_f32 v3, v3, s30, v6
	v_mul_f32_e32 v6, 0x3e000000, v11
	v_mul_f32_e64 v7, |v6|, s28
	v_exp_f32_e32 v7, v7
	v_add_f32_e32 v1, v1, v3
	v_sub_f32_e32 v3, v4, v3
	v_cndmask_b32_e64 v119, v194, v3, s[68:69]
	v_add_f32_e32 v4, 1.0, v7
	v_cndmask_b32_e64 v122, 0, -v1, s[68:69]
	v_max_f32_e32 v1, 0, v6
	v_log_f32_e32 v4, v4
	v_min_f32_e32 v6, 0, v6
	v_mul_f32_e32 v3, 0x3f317217, v4
	v_fma_f32 v3, v4, s30, -v3
	v_fmac_f32_e32 v3, 0x3377d1cf, v4
	s_nop 1
	v_fma_f32 v3, v4, s30, v3
	v_mul_f32_e32 v4, 0x3e000000, v12
	v_mul_f32_e64 v7, |v4|, s28
	v_exp_f32_e32 v7, v7
	v_add_f32_e32 v1, v1, v3
	v_sub_f32_e32 v3, v6, v3
	v_cndmask_b32_e64 v12, v194, v3, s[70:71]
	v_add_f32_e32 v6, 1.0, v7
	v_cndmask_b32_e64 v123, 0, -v1, s[70:71]
	v_max_f32_e32 v1, 0, v4
	v_log_f32_e32 v6, v6
	v_min_f32_e32 v4, 0, v4
	v_mul_f32_e32 v3, 0x3f317217, v6
	v_fma_f32 v3, v6, s30, -v3
	v_fmac_f32_e32 v3, 0x3377d1cf, v6
	s_nop 1
	v_fma_f32 v3, v6, s30, v3
	v_mul_f32_e32 v6, 0x3e000000, v13
	v_mul_f32_e64 v7, |v6|, s28
	v_exp_f32_e32 v7, v7
	v_add_f32_e32 v1, v1, v3
	v_sub_f32_e32 v3, v4, v3
	v_cndmask_b32_e64 v13, v194, v3, s[72:73]
	v_add_f32_e32 v4, 1.0, v7
	v_max_f32_e32 v3, 0, v6
	v_min_f32_e32 v6, 0, v6
	v_log_f32_e32 v4, v4
	v_cndmask_b32_e64 v1, 0, -v1, s[72:73]
	v_mul_f32_e32 v7, 0x3f317217, v4
	v_fma_f32 v7, v4, s30, -v7
	v_fmac_f32_e32 v7, 0x3377d1cf, v4
	s_nop 1
	v_fma_f32 v4, v4, s30, v7
	v_mul_f32_e32 v7, 0x3e000000, v14
	v_mul_f32_e64 v8, |v7|, s28
	v_exp_f32_e32 v8, v8
	v_add_f32_e32 v3, v3, v4
	v_sub_f32_e32 v4, v6, v4
	v_cndmask_b32_e64 v14, v194, v4, s[74:75]
	v_add_f32_e32 v6, 1.0, v8
	v_cndmask_b32_e64 v124, 0, -v3, s[74:75]
	v_max_f32_e32 v3, 0, v7
	v_log_f32_e32 v6, v6
	v_min_f32_e32 v7, 0, v7
	v_mul_f32_e32 v4, 0x3f317217, v6
	v_fma_f32 v4, v6, s30, -v4
	v_fmac_f32_e32 v4, 0x3377d1cf, v6
	s_nop 1
	v_fma_f32 v4, v6, s30, v4
	v_mul_f32_e32 v6, 0x3e000000, v15
	v_mul_f32_e64 v8, |v6|, s28
	v_exp_f32_e32 v8, v8
	v_add_f32_e32 v3, v3, v4
	v_sub_f32_e32 v4, v7, v4
	v_cndmask_b32_e64 v15, v194, v4, s[76:77]
	v_add_f32_e32 v7, 1.0, v8
	v_cndmask_b32_e64 v125, 0, -v3, s[76:77]
	v_max_f32_e32 v3, 0, v6
	v_log_f32_e32 v7, v7
	v_min_f32_e32 v6, 0, v6
	v_mul_f32_e32 v4, 0x3f317217, v7
	v_fma_f32 v4, v7, s30, -v4
	v_fmac_f32_e32 v4, 0x3377d1cf, v7
	s_nop 1
	v_fma_f32 v4, v7, s30, v4
	v_add_f32_e32 v3, v3, v4
	v_sub_f32_e32 v4, v6, v4
	v_cndmask_b32_e64 v126, v194, v4, s[78:79]
	v_cndmask_b32_e64 v127, 0, -v3, s[78:79]
	v_add_f32_e32 v3, v81, v87
	v_add_f32_e32 v4, v89, v93
	v_add_f32_e32 v4, v3, v4
	v_add_f32_e32 v3, v1, v124
	v_add_f32_e32 v1, v125, v127
	v_pk_add_f32 v[2:3], v[2:3], v[0:1]
	ds_bpermute_b32 v7, v184, v3
	v_add_f32_e32 v6, v122, v123
	v_add_f32_e32 v1, v5, v112
	v_add_f32_e32 v5, v114, v116
	ds_bpermute_b32 v8, v184, v4
	s_waitcnt lgkmcnt(0)
	v_pk_add_f32 v[2:3], v[2:3], v[6:7]
	ds_bpermute_b32 v144, v184, v2
	v_add_f32_e32 v6, v1, v5
	ds_bpermute_b32 v10, v184, v6
	v_add_f32_e32 v1, 0, v7
	v_cndmask_b32_e64 v1, 0, v1, s[42:43]
	s_waitcnt lgkmcnt(0)
	v_pk_add_f32 v[2:3], v[2:3], v[144:145]
	v_cndmask_b32_e64 v5, 0, v144, s[42:43]
	v_mov_b32_e32 v7, v2
	v_mov_b32_e32 v11, v3
	v_add_f32_e32 v81, v5, v3
	s_waitcnt lgkmcnt(0)
	v_cndmask_b32_e64 v5, 0, v10, s[42:43]
	v_pk_add_f32 v[2:3], v[6:7], v[10:11]
	v_cndmask_b32_e64 v7, 0, v8, s[42:43]
	v_add_f32_e32 v6, v5, v3
	v_mov_b32_e32 v5, v2
	v_mov_b32_e32 v9, v3
	v_pk_add_f32 v[120:121], v[4:5], v[8:9]
	v_add_f32_e32 v10, v12, v81
	v_add_f32_e32 v2, v7, v121
	v_add_f32_e32 v3, v91, v2
	v_add_f32_e32 v2, v93, v2
	v_mul_f32_e32 v10, 0x3fb8aa3b, v10
	v_add_f32_e32 v4, v79, v2
	v_exp_f32_e32 v79, v10
	v_add_f32_e32 v10, v123, v81
	v_add_f32_e32 v11, v119, v10
	v_add_f32_e32 v10, v122, v10
	v_add_f32_e32 v0, v0, v10
	v_add_f32_e32 v0, v117, v0
	v_add_f32_e32 v2, v89, v2
	v_add_f32_e32 v7, v115, v6
	v_add_f32_e32 v6, v116, v6
	v_mul_f32_e32 v0, 0x3fb8aa3b, v0
	v_add_f32_e32 v5, v85, v2
	v_add_f32_e32 v8, v113, v6
	v_add_f32_e32 v6, v114, v6
	v_exp_f32_e32 v85, v0
	v_add_f32_e32 v0, v126, v1
	v_add_f32_e32 v2, v87, v2
	v_add_f32_e32 v9, v97, v6
	v_add_f32_e32 v6, v112, v6
	v_mul_f32_e32 v0, 0x3fb8aa3b, v0
	v_add_f32_e32 v2, v83, v2
	v_add_f32_e32 v6, v95, v6
	v_exp_f32_e32 v87, v0
	v_add_f32_e32 v0, v127, v1
	v_mul_f32_e32 v3, 0x3fb8aa3b, v3
	v_mul_f32_e32 v4, 0x3fb8aa3b, v4
	v_mul_f32_e32 v5, 0x3fb8aa3b, v5
	v_mul_f32_e32 v2, 0x3fb8aa3b, v2
	v_mul_f32_e32 v7, 0x3fb8aa3b, v7
	v_mul_f32_e32 v8, 0x3fb8aa3b, v8
	v_mul_f32_e32 v9, 0x3fb8aa3b, v9
	v_mul_f32_e32 v6, 0x3fb8aa3b, v6
	v_add_f32_e32 v1, v15, v0
	v_exp_f32_e32 v3, v3
	v_exp_f32_e32 v4, v4
	v_exp_f32_e32 v5, v5
	v_exp_f32_e32 v2, v2
	v_exp_f32_e32 v7, v7
	v_exp_f32_e32 v8, v8
	v_exp_f32_e32 v9, v9
	v_exp_f32_e32 v6, v6
	v_mul_f32_e32 v1, 0x3fb8aa3b, v1
	v_add_f32_e32 v0, v125, v0
	v_mul_f32_e32 v11, 0x3fb8aa3b, v11
	v_exp_f32_e32 v89, v1
	v_add_f32_e32 v1, v14, v0
	v_add_f32_e32 v0, v124, v0
	v_exp_f32_e32 v81, v11
	v_add_f32_e32 v11, v118, v10
	v_add_f32_e32 v0, v13, v0
	v_mul_f32_e32 v11, 0x3fb8aa3b, v11
	v_mul_f32_e32 v1, 0x3fb8aa3b, v1
	v_mul_f32_e32 v0, 0x3fb8aa3b, v0
	v_exp_f32_e32 v83, v11
	v_exp_f32_e32 v91, v1
	v_exp_f32_e32 v93, v0
	s_nop 15
	s_nop 15
	v_cvt_pk_bf16_f32 v113, v4, v3
	v_cvt_pk_bf16_f32 v112, v2, v5
	v_cvt_pk_bf16_f32 v115, v8, v7
	v_cvt_pk_bf16_f32 v114, v6, v9
	s_waitcnt vmcnt(19)
	v_perm_b32 v3, v29, v28, s38
	v_perm_b32 v2, v27, v23, s38
	v_perm_b32 v1, v22, v21, s38
	s_waitcnt vmcnt(7)
	v_perm_b32 v0, v19, v31, s38
	v_perm_b32 v21, v26, v25, s38
	v_perm_b32 v20, v24, v20, s38
	v_perm_b32 v19, v18, v17, s38
	s_waitcnt vmcnt(6)
	v_perm_b32 v18, v16, v30, s38
	v_mfma_f32_32x32x16_bf16 v[0:15], v[112:115], v[0:3], 0
	s_waitcnt vmcnt(1)
	v_perm_b32 v119, v47, v46, s38
	v_perm_b32 v118, v45, v41, s38
	v_perm_b32 v117, v40, v39, s38
	v_perm_b32 v116, v37, v33, s38
	s_waitcnt vmcnt(0)
	v_perm_b32 v39, v44, v43, s38
	v_perm_b32 v38, v42, v38, s38
	v_perm_b32 v37, v36, v35, s38
	v_mfma_f32_32x32x16_bf16 v[16:31], v[112:115], v[18:21], 0
	v_cvt_pk_bf16_f32 v113, v81, v79
	v_cvt_pk_bf16_f32 v112, v85, v83
	v_cvt_pk_bf16_f32 v115, v89, v87
	v_cvt_pk_bf16_f32 v114, v93, v91
	v_perm_b32 v36, v34, v32, s38
	v_add_f32_e32 v95, v120, v121
	v_mfma_f32_32x32x16_bf16 v[0:15], v[112:115], v[116:119], v[0:15]
	v_mfma_f32_32x32x16_bf16 v[16:31], v[112:115], v[36:39], v[16:31]
	s_nop 15
	s_nop 15
	v_cmp_gt_f32_e32 vcc, s34, v95
	s_cmp_eq_u64 vcc, exec
	s_cselect_b64 s[6:7], -1, 0
	s_cmp_eq_u32 s22, 0
	s_cselect_b64 s[24:25], -1, 0
	s_or_b64 s[6:7], s[24:25], s[6:7]
	s_and_b64 vcc, exec, s[6:7]
	s_cbranch_vccnz .LBB0_256
	s_and_b32 s6, s14, 0xfe0
	s_sub_i32 s6, s6, 32
	s_add_u32 s6, s6, s10
	s_addc_u32 s7, 0, s11
	v_lshl_add_u64 v[32:33], s[6:7], 0, v[66:67]
	v_mad_u64_u32 v[112:113], s[10:11], v32, s27, v[106:107]
	v_mad_i32_i24 v113, v33, s27, v113
	v_lshl_add_u64 v[32:33], s[6:7], 0, v[64:65]
	v_mad_u64_u32 v[114:115], s[6:7], v32, s27, v[108:109]
	s_mov_b32 s24, 0xfffdc000
	v_mad_i32_i24 v115, v33, s27, v115
	s_mov_b32 s25, -1
.LBB0_255:
	v_lshl_add_u64 v[36:37], v[114:115], 0, v[98:99]
	global_load_dwordx4 v[32:35], v[36:37], off offset:-64
	global_load_dwordx4 v[116:119], v[36:37], off offset:-32
	global_load_dwordx4 v[120:123], v[36:37], off
	global_load_dwordx4 v[124:127], v[36:37], off offset:32
	v_lshl_add_u64 v[36:37], v[112:113], 0, v[98:99]
	v_add_co_u32_e32 v38, vcc, 0x8640000, v36
	s_sub_i32 s10, s22, 32
	s_nop 0
	v_addc_co_u32_e32 v39, vcc, 0, v37, vcc
	v_add_co_u32_e32 v40, vcc, 0x8641000, v36
	s_nop 1
	v_addc_co_u32_e32 v41, vcc, 0, v37, vcc
	v_add_co_u32_e32 v42, vcc, 0x8643000, v36
	s_nop 1
	v_addc_co_u32_e32 v43, vcc, 0, v37, vcc
	v_add_co_u32_e32 v44, vcc, 0x8644000, v36
	s_nop 1
	v_addc_co_u32_e32 v45, vcc, 0, v37, vcc
	global_load_ushort v85, v[38:39], off offset:3072
	global_load_ushort v79, v[38:39], off offset:3136
	global_load_ushort v89, v[40:41], off offset:3584
	global_load_ushort v81, v[40:41], off offset:3648
	global_load_ushort v91, v[42:43], off
	global_load_ushort v83, v[42:43], off offset:64
	global_load_ushort v93, v[44:45], off offset:512
	global_load_ushort v87, v[44:45], off offset:576
	v_add_co_u32_e32 v38, vcc, 0x8649000, v36
	s_nop 1
	v_addc_co_u32_e32 v39, vcc, 0, v37, vcc
	v_add_co_u32_e32 v40, vcc, 0x864a000, v36
	s_nop 1
	v_addc_co_u32_e32 v41, vcc, 0, v37, vcc
	v_add_co_u32_e32 v42, vcc, 0x864c000, v36
	s_nop 1
	v_addc_co_u32_e32 v43, vcc, 0, v37, vcc
	v_add_co_u32_e32 v44, vcc, 0x864d000, v36
	s_nop 1
	v_addc_co_u32_e32 v45, vcc, 0, v37, vcc
	global_load_ushort v139, v[38:39], off offset:3072
	global_load_ushort v97, v[38:39], off offset:3136
	global_load_ushort v142, v[40:41], off offset:3584
	global_load_ushort v136, v[40:41], off offset:3648
	global_load_ushort v144, v[42:43], off
	global_load_ushort v137, v[42:43], off offset:64
	global_load_ushort v154, v[44:45], off offset:512
	global_load_ushort v140, v[44:45], off offset:576
	v_add_co_u32_e32 v38, vcc, 0x8652000, v36
	s_nop 1
	v_addc_co_u32_e32 v39, vcc, 0, v37, vcc
	v_add_co_u32_e32 v40, vcc, 0x8653000, v36
	s_nop 1
	v_addc_co_u32_e32 v41, vcc, 0, v37, vcc
	v_add_co_u32_e32 v42, vcc, 0x8655000, v36
	s_nop 1
	v_addc_co_u32_e32 v43, vcc, 0, v37, vcc
	v_add_co_u32_e32 v44, vcc, 0x8656000, v36
	s_nop 1
	v_addc_co_u32_e32 v45, vcc, 0, v37, vcc
	global_load_ushort v152, v[38:39], off offset:3072
	global_load_ushort v138, v[38:39], off offset:3136
	global_load_ushort v155, v[40:41], off offset:3584
	global_load_ushort v141, v[40:41], off offset:3648
	global_load_ushort v156, v[42:43], off
	global_load_ushort v143, v[42:43], off offset:64
	global_load_ushort v157, v[44:45], off offset:512
	global_load_ushort v153, v[44:45], off offset:576
	v_add_co_u32_e32 v38, vcc, 0x865b000, v36
	s_nop 1
	v_addc_co_u32_e32 v39, vcc, 0, v37, vcc
	v_add_co_u32_e32 v40, vcc, 0x865c000, v36
	s_nop 1
	v_addc_co_u32_e32 v41, vcc, 0, v37, vcc
	v_add_co_u32_e32 v42, vcc, 0x865e000, v36
	s_nop 1
	v_addc_co_u32_e32 v43, vcc, 0, v37, vcc
	v_add_co_u32_e32 v36, vcc, 0x865f000, v36
	s_nop 1
	v_addc_co_u32_e32 v37, vcc, 0, v37, vcc
	global_load_ushort v161, v[38:39], off offset:3072
	global_load_ushort v158, v[38:39], off offset:3136
	global_load_ushort v163, v[40:41], off offset:3584
	global_load_ushort v159, v[40:41], off offset:3648
	global_load_ushort v164, v[42:43], off
	global_load_ushort v160, v[42:43], off offset:64
	global_load_ushort v165, v[36:37], off offset:512
	global_load_ushort v162, v[36:37], off offset:576
	s_nop 15
	s_nop 15
	s_waitcnt vmcnt(35)
	v_mfma_f32_32x32x16_bf16 v[32:47], v[32:35], v[48:51], 0
	s_waitcnt vmcnt(34)
	v_mfma_f32_32x32x16_bf16 v[32:47], v[116:119], v[52:55], v[32:47]
	s_waitcnt vmcnt(33)
	v_mfma_f32_32x32x16_bf16 v[32:47], v[120:123], v[56:59], v[32:47]
	s_waitcnt vmcnt(32)
	v_mfma_f32_32x32x16_bf16 v[32:47], v[124:127], v[60:63], v[32:47]
	s_nop 15
	s_nop 15
	s_nop 11
	v_mul_f32_e32 v117, 0x3e000000, v32
	v_mul_f32_e64 v32, |v117|, s28
	v_exp_f32_e32 v32, v32
	v_mul_f32_e32 v33, 0x3e000000, v33
	v_mul_f32_e32 v121, 0x3e000000, v34
	v_mul_f32_e64 v34, |v121|, s28
	v_add_f32_e32 v32, 1.0, v32
	v_exp_f32_e32 v34, v34
	v_max_f32_e32 v122, 0, v117
	v_log_f32_e32 v32, v32
	v_mul_f32_e64 v116, |v33|, s28
	v_exp_f32_e32 v116, v116
	v_mul_f32_e32 v119, 0x3f317217, v32
	v_fma_f32 v119, v32, s30, -v119
	v_fmac_f32_e32 v119, 0x3377d1cf, v32
	v_add_f32_e32 v116, 1.0, v116
	v_add_f32_e32 v34, 1.0, v34
	v_fma_f32 v32, v32, s30, v119
	v_cmp_gt_f32_e32 vcc, s29, v116
	v_max_f32_e32 v124, 0, v33
	s_nop 0
	v_cndmask_b32_e64 v119, 0, 32, vcc
	v_ldexp_f32 v116, v116, v119
	v_log_f32_e32 v119, v116
	v_min_f32_e32 v116, 0, v117
	v_cndmask_b32_e32 v118, 0, v193, vcc
	v_cmp_gt_f32_e32 vcc, s29, v34
	v_mul_f32_e32 v117, 0x3f317217, v119
	v_fma_f32 v117, v119, s30, -v117
	v_fmac_f32_e32 v117, 0x3377d1cf, v119
	v_fmac_f32_e32 v117, 0x3f317217, v119
	v_cmp_lt_f32_e64 s[6:7], |v119|, s31
	v_mul_f32_e32 v36, 0x3e000000, v36
	v_max_f32_e32 v123, 0, v121
	v_cndmask_b32_e64 v117, v119, v117, s[6:7]
	v_cndmask_b32_e64 v119, 0, 32, vcc
	v_ldexp_f32 v34, v34, v119
	v_log_f32_e32 v119, v34
	v_sub_f32_e32 v34, v117, v118
	v_mul_f32_e32 v117, 0x3e000000, v35
	v_mul_f32_e64 v35, |v117|, s28
	v_exp_f32_e32 v35, v35
	v_min_f32_e32 v118, 0, v33
	v_mul_f32_e32 v33, 0x3f317217, v119
	v_fma_f32 v33, v119, s30, -v33
	v_fmac_f32_e32 v33, 0x3377d1cf, v119
	v_fmac_f32_e32 v33, 0x3f317217, v119
	v_cmp_lt_f32_e64 s[6:7], |v119|, s31
	v_add_f32_e32 v35, 1.0, v35
	v_max_f32_e32 v125, 0, v117
	v_cndmask_b32_e64 v33, v119, v33, s[6:7]
	v_cndmask_b32_e32 v119, 0, v193, vcc
	v_sub_f32_e32 v33, v33, v119
	v_mul_f32_e32 v37, 0x3e000000, v37
	v_log_f32_e32 v35, v35
	v_min_f32_e32 v120, 0, v121
	v_mul_f32_e64 v121, |v36|, s28
	v_exp_f32_e32 v121, v121
	v_mul_f32_e32 v119, 0x3f317217, v35
	v_fma_f32 v119, v35, s30, -v119
	v_fmac_f32_e32 v119, 0x3377d1cf, v35
	v_mul_f32_e32 v39, 0x3e000000, v39
	v_mul_f32_e32 v41, 0x3e000000, v41
	v_fma_f32 v35, v35, s30, v119
	v_add_f32_e32 v119, 1.0, v121
	v_min_f32_e32 v132, 0, v41
	v_max_f32_e32 v168, 0, v41
	v_log_f32_e32 v119, v119
	v_min_f32_e32 v121, 0, v117
	v_sub_f32_e32 v131, v121, v35
	v_mul_f32_e32 v117, 0x3f317217, v119
	v_fma_f32 v117, v119, s30, -v117
	v_fmac_f32_e32 v117, 0x3377d1cf, v119
	v_mul_f32_e32 v45, 0x3e000000, v45
	v_min_f32_e32 v176, 0, v45
	v_fma_f32 v117, v119, s30, v117
	v_mul_f32_e64 v119, |v37|, s28
	v_exp_f32_e32 v119, v119
	v_min_f32_e32 v121, 0, v36
	v_sub_f32_e32 v133, v121, v117
	v_add_f32_e32 v119, 1.0, v119
	v_mul_f32_e32 v121, 0x3e000000, v38
	v_mul_f32_e64 v38, |v121|, s28
	v_log_f32_e32 v119, v119
	v_max_f32_e32 v36, 0, v36
	v_exp_f32_e32 v38, v38
	v_add_f32_e32 v117, v36, v117
	v_mul_f32_e32 v36, 0x3f317217, v119
	v_fma_f32 v36, v119, s30, -v36
	v_fmac_f32_e32 v36, 0x3377d1cf, v119
	v_add_f32_e32 v38, 1.0, v38
	v_mul_f32_e64 v126, |v39|, s28
	v_fma_f32 v36, v119, s30, v36
	v_cmp_gt_f32_e32 vcc, s29, v38
	v_exp_f32_e32 v127, v126
	s_nop 0
	v_cndmask_b32_e64 v119, 0, 32, vcc
	v_ldexp_f32 v38, v38, v119
	v_log_f32_e32 v119, v38
	v_min_f32_e32 v38, 0, v37
	v_max_f32_e32 v37, 0, v37
	v_add_f32_e32 v171, v37, v36
	v_mul_f32_e32 v37, 0x3f317217, v119
	v_fma_f32 v37, v119, s30, -v37
	v_fmac_f32_e32 v37, 0x3377d1cf, v119
	v_fmac_f32_e32 v37, 0x3f317217, v119
	v_cmp_lt_f32_e64 s[6:7], |v119|, s31
	v_min_f32_e32 v128, 0, v121
	v_max_f32_e32 v178, 0, v45
	v_cndmask_b32_e64 v37, v119, v37, s[6:7]
	v_cndmask_b32_e32 v119, 0, v193, vcc
	v_sub_f32_e32 v126, v37, v119
	v_add_f32_e32 v37, 1.0, v127
	v_cmp_gt_f32_e32 vcc, s29, v37
	v_pk_add_f32 v[124:125], v[124:125], v[34:35]
	v_sub_f32_e64 v206, -v171, v117
	v_cndmask_b32_e64 v119, 0, 32, vcc
	v_ldexp_f32 v37, v37, v119
	v_log_f32_e32 v119, v37
	v_max_f32_e32 v37, 0, v121
	v_cndmask_b32_e32 v127, 0, v193, vcc
	v_add_f32_e32 v37, v37, v126
	v_mul_f32_e32 v121, 0x3f317217, v119
	v_fma_f32 v121, v119, s30, -v121
	v_fmac_f32_e32 v121, 0x3377d1cf, v119
	v_fmac_f32_e32 v121, 0x3f317217, v119
	v_cmp_lt_f32_e64 s[6:7], |v119|, s31
	v_pk_add_f32 v[122:123], v[122:123], v[32:33]
	s_nop 0
	v_cndmask_b32_e64 v119, v119, v121, s[6:7]
	v_mul_f32_e32 v121, 0x3e000000, v40
	v_mul_f32_e64 v40, |v121|, s28
	v_exp_f32_e32 v40, v40
	v_sub_f32_e32 v119, v119, v127
	v_min_f32_e32 v127, 0, v39
	v_max_f32_e32 v39, 0, v39
	v_add_f32_e32 v40, 1.0, v40
	v_sub_f32_e32 v174, v127, v119
	v_add_f32_e32 v127, v39, v119
	v_log_f32_e32 v40, v40
	v_mul_f32_e64 v119, |v41|, s28
	v_exp_f32_e32 v119, v119
	v_min_f32_e32 v130, 0, v121
	v_mul_f32_e32 v39, 0x3f317217, v40
	v_fma_f32 v39, v40, s30, -v39
	v_fmac_f32_e32 v39, 0x3377d1cf, v40
	v_add_f32_e32 v119, 1.0, v119
	v_max_f32_e32 v166, 0, v121
	v_fma_f32 v39, v40, s30, v39
	v_mul_f32_e32 v121, 0x3e000000, v42
	v_mul_f32_e64 v42, |v121|, s28
	v_log_f32_e32 v119, v119
	v_exp_f32_e32 v42, v42
	v_mov_b32_e32 v40, v39
	v_min_f32_e32 v134, 0, v121
	v_mul_f32_e32 v39, 0x3f317217, v119
	v_fma_f32 v39, v119, s30, -v39
	v_fmac_f32_e32 v39, 0x3377d1cf, v119
	v_add_f32_e32 v42, 1.0, v42
	v_max_f32_e32 v167, 0, v121
	v_fma_f32 v39, v119, s30, v39
	v_cmp_gt_f32_e32 vcc, s29, v42
	v_mul_f32_e32 v121, 0x3e000000, v44
	v_min_f32_e32 v170, 0, v121
	v_cndmask_b32_e64 v129, 0, 32, vcc
	v_ldexp_f32 v42, v42, v129
	v_log_f32_e32 v129, v42
	v_mov_b32_e32 v42, v39
	v_mul_f32_e32 v119, 0x3e000000, v43
	v_mul_f32_e64 v41, |v119|, s28
	v_exp_f32_e32 v41, v41
	v_mul_f32_e32 v39, 0x3f317217, v129
	v_fma_f32 v39, v129, s30, -v39
	v_fmac_f32_e32 v39, 0x3377d1cf, v129
	v_add_f32_e32 v41, 1.0, v41
	v_fmac_f32_e32 v39, 0x3f317217, v129
	v_cmp_lt_f32_e64 s[6:7], |v129|, s31
	v_cndmask_b32_e32 v43, 0, v193, vcc
	v_cmp_gt_f32_e32 vcc, s29, v41
	v_cndmask_b32_e64 v39, v129, v39, s[6:7]
	v_max_f32_e32 v169, 0, v119
	v_cndmask_b32_e64 v129, 0, 32, vcc
	v_ldexp_f32 v41, v41, v129
	v_log_f32_e32 v129, v41
	v_sub_f32_e32 v41, v39, v43
	v_mul_f32_e64 v43, |v121|, s28
	v_exp_f32_e32 v44, v43
	v_mul_f32_e32 v39, 0x3f317217, v129
	v_fma_f32 v39, v129, s30, -v39
	v_fmac_f32_e32 v39, 0x3377d1cf, v129
	v_fmac_f32_e32 v39, 0x3f317217, v129
	v_cmp_lt_f32_e64 s[6:7], |v129|, s31
	v_cndmask_b32_e32 v43, 0, v193, vcc
	v_max_f32_e32 v172, 0, v121
	v_cndmask_b32_e64 v39, v129, v39, s[6:7]
	v_sub_f32_e32 v43, v39, v43
	v_add_f32_e32 v39, 1.0, v44
	v_mul_f32_e32 v121, 0x3e000000, v46
	v_mul_f32_e64 v46, |v121|, s28
	v_log_f32_e32 v39, v39
	v_min_f32_e32 v44, 0, v119
	v_mul_f32_e64 v119, |v45|, s28
	v_exp_f32_e32 v119, v119
	v_sub_f32_e32 v177, v44, v43
	v_mul_f32_e32 v44, 0x3f317217, v39
	v_fma_f32 v44, v39, s30, -v44
	v_fmac_f32_e32 v44, 0x3377d1cf, v39
	v_add_f32_e32 v119, 1.0, v119
	v_exp_f32_e32 v46, v46
	v_fma_f32 v39, v39, s30, v44
	v_mov_b32_e32 v44, v39
	v_add_f32_e32 v46, 1.0, v46
	v_log_f32_e32 v119, v119
	v_pk_add_f32 v[166:167], v[166:167], v[40:41]
	v_pk_add_f32 v[168:169], v[168:169], v[42:43]
	v_max_f32_e32 v173, 0, v121
	v_mul_f32_e32 v39, 0x3f317217, v119
	v_fma_f32 v39, v119, s30, -v39
	v_fmac_f32_e32 v39, 0x3377d1cf, v119
	v_pk_add_f32 v[208:209], v[168:169], v[166:167] neg_lo:[1,1] neg_hi:[1,1]
	v_sub_f32_e64 v210, -v127, v37
	v_fma_f32 v39, v119, s30, v39
	v_cmp_gt_f32_e32 vcc, s29, v46
	v_pk_add_f32 v[208:209], v[208:209], v[208:209] op_sel:[0,1] op_sel_hi:[1,0]
	ds_bpermute_b32 v211, v184, v208
	v_cndmask_b32_e64 v129, 0, 32, vcc
	v_ldexp_f32 v46, v46, v129
	v_log_f32_e32 v129, v46
	v_mov_b32_e32 v46, v39
	v_mul_f32_e32 v119, 0x3e000000, v47
	v_mul_f32_e64 v45, |v119|, s28
	v_exp_f32_e32 v45, v45
	v_mul_f32_e32 v39, 0x3f317217, v129
	v_fma_f32 v39, v129, s30, -v39
	v_fmac_f32_e32 v39, 0x3377d1cf, v129
	v_add_f32_e32 v45, 1.0, v45
	v_fmac_f32_e32 v39, 0x3f317217, v129
	v_cmp_lt_f32_e64 s[6:7], |v129|, s31
	v_cndmask_b32_e32 v47, 0, v193, vcc
	v_cmp_gt_f32_e32 vcc, s29, v45
	v_cndmask_b32_e64 v39, v129, v39, s[6:7]
	v_max_f32_e32 v179, 0, v119
	v_cndmask_b32_e64 v129, 0, 32, vcc
	v_ldexp_f32 v45, v45, v129
	v_log_f32_e32 v129, v45
	v_sub_f32_e32 v45, v39, v47
	v_cndmask_b32_e32 v47, 0, v193, vcc
	v_pk_add_f32 v[172:173], v[172:173], v[44:45]
	v_mul_f32_e32 v39, 0x3f317217, v129
	v_fma_f32 v39, v129, s30, -v39
	v_fmac_f32_e32 v39, 0x3377d1cf, v129
	v_fmac_f32_e32 v39, 0x3f317217, v129
	v_cmp_lt_f32_e64 s[6:7], |v129|, s31
	v_mov_b32_e32 v207, v208
	s_waitcnt lgkmcnt(0)
	v_pk_add_f32 v[206:207], v[206:207], v[210:211]
	v_cndmask_b32_e64 v39, v129, v39, s[6:7]
	v_sub_f32_e32 v47, v39, v47
	v_pk_add_f32 v[178:179], v[178:179], v[46:47]
	v_min_f32_e32 v39, 0, v119
	v_pk_add_f32 v[212:213], v[178:179], v[172:173] neg_lo:[1,1] neg_hi:[1,1]
	v_sub_f32_e32 v190, v39, v47
	v_add_f32_e32 v35, v212, v213
	ds_bpermute_b32 v39, v184, v35
	ds_bpermute_b32 v208, v184, v206
	v_pk_add_f32 v[182:183], v[124:125], v[122:123] neg_lo:[1,1] neg_hi:[1,1]
	v_min_f32_e32 v180, 0, v121
	v_mov_b32_e32 v212, v182
	s_waitcnt lgkmcnt(0)
	v_add_f32_e32 v35, v35, v39
	v_add_f32_e32 v209, v95, v35
	s_waitcnt lgkmcnt(0)
	v_pk_add_f32 v[206:207], v[206:207], v[208:209]
	v_cndmask_b32_e64 v43, 0, v39, s[42:43]
	v_mov_b32_e32 v213, v206
	v_mov_b32_e32 v206, v183
	v_pk_add_f32 v[182:183], v[212:213], v[206:207]
	v_add_f32_e32 v181, v95, v43
	ds_bpermute_b32 v95, v184, v182
	v_cndmask_b32_e64 v35, 0, v211, s[42:43]
	v_add_f32_e32 v135, v35, v209
	v_cndmask_b32_e64 v35, 0, v208, s[42:43]
	v_add_f32_e32 v129, v35, v207
	s_waitcnt lgkmcnt(0)
	v_cndmask_b32_e64 v35, 0, v95, s[42:43]
	v_add_f32_e32 v121, v35, v183
	v_add_f32_e32 v35, v131, v121
	v_mov_b32_e32 v206, v33
	v_mov_b32_e32 v207, v125
	v_mul_f32_e32 v35, 0x3fb8aa3b, v35
	v_pk_add_f32 v[120:121], v[120:121], v[206:207] neg_lo:[0,1] neg_hi:[0,1]
	v_exp_f32_e32 v122, v35
	v_add_f32_e32 v33, v120, v121
	v_mov_b32_e32 v119, v121
	v_mov_b32_e32 v35, v123
	v_mul_f32_e32 v33, 0x3fb8aa3b, v33
	v_pk_add_f32 v[34:35], v[118:119], v[34:35] neg_lo:[0,1] neg_hi:[0,1]
	v_exp_f32_e32 v120, v33
	v_add_f32_e32 v33, v34, v35
	v_mul_f32_e32 v33, 0x3fb8aa3b, v33
	v_exp_f32_e32 v34, v33
	v_mov_b32_e32 v117, v35
	v_mov_b32_e32 v33, v124
	v_pk_add_f32 v[32:33], v[116:117], v[32:33] neg_lo:[0,1] neg_hi:[0,1]
	v_mov_b32_e32 v43, v167
	v_add_f32_e32 v32, v32, v33
	v_mul_f32_e32 v32, 0x3fb8aa3b, v32
	v_exp_f32_e32 v35, v32
	v_add_f32_e32 v32, v174, v129
	v_mul_f32_e32 v32, 0x3fb8aa3b, v32
	v_exp_f32_e32 v116, v32
	v_pk_add_f32 v[32:33], v[128:129], v[126:127] neg_lo:[0,1] neg_hi:[0,1]
	v_mov_b32_e32 v47, v173
	v_add_f32_e32 v32, v32, v33
	v_mul_f32_e32 v32, 0x3fb8aa3b, v32
	v_mov_b32_e32 v39, v33
	v_exp_f32_e32 v117, v32
	v_pk_add_f32 v[32:33], v[38:39], v[36:37] neg_lo:[0,1] neg_hi:[0,1]
	s_nop 0
	v_add_f32_e32 v32, v32, v33
	v_mul_f32_e32 v32, 0x3fb8aa3b, v32
	v_exp_f32_e32 v36, v32
	v_sub_f32_e32 v32, v33, v171
	v_add_f32_e32 v32, v133, v32
	v_mul_f32_e32 v32, 0x3fb8aa3b, v32
	v_exp_f32_e32 v37, v32
	v_add_f32_e32 v32, v177, v135
	v_mul_f32_e32 v32, 0x3fb8aa3b, v32
	v_exp_f32_e32 v118, v32
	v_mov_b32_e32 v32, v41
	v_mov_b32_e32 v33, v169
	v_pk_add_f32 v[32:33], v[134:135], v[32:33] neg_lo:[0,1] neg_hi:[0,1]
	v_mov_b32_e32 v41, v168
	v_add_f32_e32 v32, v32, v33
	v_mul_f32_e32 v32, 0x3fb8aa3b, v32
	v_mov_b32_e32 v133, v33
	v_exp_f32_e32 v119, v32
	v_pk_add_f32 v[32:33], v[132:133], v[42:43] neg_lo:[0,1] neg_hi:[0,1]
	s_nop 0
	v_add_f32_e32 v32, v32, v33
	v_mul_f32_e32 v32, 0x3fb8aa3b, v32
	v_mov_b32_e32 v131, v33
	v_exp_f32_e32 v42, v32
	v_pk_add_f32 v[32:33], v[130:131], v[40:41] neg_lo:[0,1] neg_hi:[0,1]
	s_nop 0
	v_add_f32_e32 v32, v32, v33
	v_mul_f32_e32 v32, 0x3fb8aa3b, v32
	v_exp_f32_e32 v40, v32
	v_add_f32_e32 v32, v190, v181
	v_mul_f32_e32 v32, 0x3fb8aa3b, v32
	v_exp_f32_e32 v41, v32
	v_mov_b32_e32 v32, v45
	v_mov_b32_e32 v33, v179
	v_pk_add_f32 v[32:33], v[180:181], v[32:33] neg_lo:[0,1] neg_hi:[0,1]
	v_mov_b32_e32 v45, v178
	v_add_f32_e32 v32, v32, v33
	v_mul_f32_e32 v32, 0x3fb8aa3b, v32
	v_mov_b32_e32 v177, v33
	v_exp_f32_e32 v43, v32
	v_pk_add_f32 v[32:33], v[176:177], v[46:47] neg_lo:[0,1] neg_hi:[0,1]
	s_nop 0
	v_add_f32_e32 v32, v32, v33
	v_mul_f32_e32 v32, 0x3fb8aa3b, v32
	v_mov_b32_e32 v171, v33
	v_exp_f32_e32 v46, v32
	v_pk_add_f32 v[32:33], v[170:171], v[44:45] neg_lo:[0,1] neg_hi:[0,1]
	v_add_f32_e32 v45, v182, v95
	v_add_f32_e32 v32, v32, v33
	v_mul_f32_e32 v32, 0x3fb8aa3b, v32
	v_exp_f32_e32 v44, v32
	s_nop 15
	s_nop 15
	v_cvt_pk_bf16_f32 v32, v35, v34
	v_cvt_pk_bf16_f32 v33, v120, v122
	v_cvt_pk_bf16_f32 v35, v117, v116
	v_cvt_pk_bf16_f32 v34, v37, v36
	s_waitcnt vmcnt(17)
	v_perm_b32 v39, v154, v144, s38
	v_perm_b32 v38, v142, v139, s38
	v_perm_b32 v37, v93, v91, s38
	v_perm_b32 v36, v89, v85, s38
	v_add_f32_e32 v95, v45, v183
	s_nop 0
	v_mfma_f32_32x32x16_bf16 v[0:15], v[32:35], v[36:39], v[0:15]
	s_waitcnt vmcnt(16)
	v_perm_b32 v39, v140, v137, s38
	v_perm_b32 v38, v136, v97, s38
	v_perm_b32 v37, v87, v83, s38
	v_perm_b32 v36, v81, v79, s38
	s_nop 1
	v_mfma_f32_32x32x16_bf16 v[16:31], v[32:35], v[36:39], v[16:31]
	v_cvt_pk_bf16_f32 v32, v40, v42
	v_cvt_pk_bf16_f32 v33, v119, v118
	v_cvt_pk_bf16_f32 v34, v44, v46
	v_cvt_pk_bf16_f32 v35, v43, v41
	s_waitcnt vmcnt(1)
	v_perm_b32 v39, v165, v164, s38
	v_perm_b32 v38, v163, v161, s38
	v_perm_b32 v37, v157, v156, s38
	v_perm_b32 v36, v155, v152, s38
	s_nop 1
	v_mfma_f32_32x32x16_bf16 v[0:15], v[32:35], v[36:39], v[0:15]
	s_waitcnt vmcnt(0)
	v_perm_b32 v39, v162, v160, s38
	v_perm_b32 v38, v159, v158, s38
	v_perm_b32 v37, v153, v143, s38
	v_perm_b32 v36, v141, v138, s38
	s_nop 1
	v_mfma_f32_32x32x16_bf16 v[16:31], v[32:35], v[36:39], v[16:31]
	s_nop 15
	s_nop 15
	v_cmp_gt_f32_e32 vcc, s34, v95
	s_cmp_lg_u64 vcc, exec
	s_cselect_b64 s[6:7], -1, 0
	s_cmp_gt_u32 s22, 63
	s_mov_b32 s22, s10
	s_cselect_b64 s[10:11], -1, 0
	s_and_b64 s[6:7], s[10:11], s[6:7]
	v_lshl_add_u64 v[112:113], v[112:113], 0, s[24:25]
	v_lshl_add_u64 v[114:115], v[114:115], 0, s[24:25]
	s_and_b64 vcc, exec, s[6:7]
	s_cbranch_vccnz .LBB0_255

.LBB0_759:
	s_or_b64 exec, exec, s[6:7]
	v_readlane_b32 s8, v255, 42
	v_readlane_b32 s9, v255, 43
	s_mov_b64 s[6:7], -1
	s_and_b64 vcc, exec, s[8:9]
	s_waitcnt lgkmcnt(0)
	s_barrier
	s_cbranch_vccz .LBB0_766
	v_readlane_b32 s10, v253, 0
	v_readlane_b32 s11, v253, 1
	v_mov_b32_e32 v3, v175
	v_readlane_b32 s6, v253, 8
	v_ashrrev_i32_e32 v0, 6, v3
	s_nop 0
	v_add_u32_e32 v0, s6, v0
	v_cmp_gt_i32_e32 vcc, s87, v0
	s_and_saveexec_b64 s[6:7], vcc
	s_mov_b32 s18, 0x800000
	s_cbranch_execz .LBB0_765
	v_ashrrev_i32_e32 v1, 31, v0
	v_and_b32_e32 v2, 15, v3
	v_lshlrev_b64 v[34:35], 9, v[0:1]
	v_lshl_add_u64 v[4:5], s[94:95], 0, v[34:35]
	v_lshlrev_b32_e32 v144, 2, v2
	v_lshl_add_u64 v[4:5], v[4:5], 0, v[144:145]
	global_load_dword v92, v[4:5], off
	v_readlane_b32 s12, v255, 7
	v_readlane_b32 s13, v255, 8
	s_lshl_b64 s[8:9], s[12:13], 17
	s_add_u32 s8, s88, s8
	s_addc_u32 s9, s89, s9
	s_lshl_b64 s[14:15], s[12:13], 23
	v_readlane_b32 s12, v253, 29
	v_readlane_b32 s13, v253, 30
	s_add_u32 s12, s12, s14
	v_and_b32_e32 v28, 63, v3
	s_addc_u32 s13, s13, s15
	v_readlane_b32 s16, v253, 27
	v_lshlrev_b32_e32 v144, 3, v28
	v_readlane_b32 s17, v253, 28
	s_add_u32 s14, s16, s14
	v_lshl_add_u64 v[6:7], s[12:13], 0, v[144:145]
	s_addc_u32 s15, s17, s15
	v_lshl_add_u64 v[4:5], s[14:15], 0, v[144:145]
	s_load_dwordx2 s[10:11], s[10:11], 0xf0
	v_lshlrev_b32_e32 v144, 5, v28
	v_and_b32_e32 v1, 32, v3
	v_cmp_eq_u32_e64 s[40:41], 0, v1
	v_and_b32_e32 v1, 16, v3
	v_and_b32_e32 v93, 60, v3
	v_cmp_eq_u32_e64 s[42:43], 0, v1
	v_and_b32_e32 v1, 8, v3
	v_cmp_eq_u32_e64 s[44:45], 0, v1
	v_and_b32_e32 v1, 4, v3
	v_or_b32_e32 v34, v34, v93
	v_cmp_eq_u32_e64 s[46:47], 0, v1
	s_waitcnt vmcnt(0)
	v_readlane_b32 s12, v92, 0
	s_ashr_i32 s13, s12, 31
	s_lshl_b64 s[12:13], s[12:13], 9
	v_lshl_add_u64 v[8:9], v[4:5], 0, s[12:13]
	v_lshl_add_u64 v[10:11], v[6:7], 0, s[12:13]
	v_readlane_b32 s12, v92, 1
	s_ashr_i32 s13, s12, 31
	s_lshl_b64 s[12:13], s[12:13], 9
	v_lshl_add_u64 v[12:13], v[6:7], 0, s[12:13]
	global_load_dwordx2 v[8:9], v[8:9], off
	s_nop 0
	global_load_dwordx2 v[82:83], v[10:11], off
	global_load_dwordx2 v[80:81], v[12:13], off
	v_lshl_add_u64 v[10:11], v[4:5], 0, s[12:13]
	v_readlane_b32 s12, v92, 2
	s_ashr_i32 s13, s12, 31
	s_lshl_b64 s[12:13], s[12:13], 9
	v_lshl_add_u64 v[12:13], v[4:5], 0, s[12:13]
	v_lshl_add_u64 v[14:15], v[6:7], 0, s[12:13]
	v_readlane_b32 s12, v92, 3
	s_ashr_i32 s13, s12, 31
	s_lshl_b64 s[12:13], s[12:13], 9
	v_lshl_add_u64 v[16:17], v[6:7], 0, s[12:13]
	global_load_dwordx2 v[10:11], v[10:11], off
	s_nop 0
	global_load_dwordx2 v[12:13], v[12:13], off
	s_nop 0
	global_load_dwordx2 v[78:79], v[14:15], off
	global_load_dwordx2 v[76:77], v[16:17], off
	v_lshl_add_u64 v[14:15], v[4:5], 0, s[12:13]
	v_readlane_b32 s12, v92, 4
	s_ashr_i32 s13, s12, 31
	s_lshl_b64 s[12:13], s[12:13], 9
	v_lshl_add_u64 v[16:17], v[4:5], 0, s[12:13]
	v_lshl_add_u64 v[18:19], v[6:7], 0, s[12:13]
	v_readlane_b32 s12, v92, 5
	s_ashr_i32 s13, s12, 31
	s_lshl_b64 s[12:13], s[12:13], 9
	v_lshl_add_u64 v[20:21], v[6:7], 0, s[12:13]
	global_load_dwordx2 v[14:15], v[14:15], off
	s_nop 0
	global_load_dwordx2 v[16:17], v[16:17], off
	s_nop 0
	global_load_dwordx2 v[74:75], v[18:19], off
	global_load_dwordx2 v[70:71], v[20:21], off
	v_lshl_add_u64 v[18:19], v[4:5], 0, s[12:13]
	v_readlane_b32 s12, v92, 6
	s_ashr_i32 s13, s12, 31
	s_lshl_b64 s[12:13], s[12:13], 9
	v_lshl_add_u64 v[20:21], v[4:5], 0, s[12:13]
	v_lshl_add_u64 v[22:23], v[6:7], 0, s[12:13]
	v_readlane_b32 s12, v92, 7
	s_ashr_i32 s13, s12, 31
	s_lshl_b64 s[12:13], s[12:13], 9
	v_lshl_add_u64 v[24:25], v[6:7], 0, s[12:13]
	global_load_dwordx2 v[18:19], v[18:19], off
	s_nop 0
	global_load_dwordx2 v[20:21], v[20:21], off
	s_nop 0
	global_load_dwordx2 v[68:69], v[22:23], off
	global_load_dwordx2 v[64:65], v[24:25], off
	v_lshl_add_u64 v[22:23], v[4:5], 0, s[12:13]
	v_readlane_b32 s12, v92, 8
	s_ashr_i32 s13, s12, 31
	s_lshl_b64 s[12:13], s[12:13], 9
	v_lshl_add_u64 v[24:25], v[4:5], 0, s[12:13]
	v_lshl_add_u64 v[26:27], v[6:7], 0, s[12:13]
	v_readlane_b32 s12, v92, 9
	s_ashr_i32 s13, s12, 31
	s_lshl_b64 s[12:13], s[12:13], 9
	global_load_dwordx2 v[22:23], v[22:23], off
	s_nop 0
	global_load_dwordx2 v[24:25], v[24:25], off
	s_nop 0
	global_load_dwordx2 v[62:63], v[26:27], off
	v_lshl_add_u64 v[26:27], v[4:5], 0, s[12:13]
	global_load_dwordx2 v[38:39], v[26:27], off
	v_lshl_add_u64 v[26:27], v[6:7], 0, s[12:13]
	v_readlane_b32 s12, v92, 10
	s_ashr_i32 s13, s12, 31
	s_lshl_b64 s[12:13], s[12:13], 9
	global_load_dwordx2 v[66:67], v[26:27], off
	v_lshl_add_u64 v[26:27], v[4:5], 0, s[12:13]
	global_load_dwordx2 v[50:51], v[26:27], off
	v_lshl_add_u64 v[26:27], v[6:7], 0, s[12:13]
	v_readlane_b32 s12, v92, 11
	s_ashr_i32 s13, s12, 31
	s_lshl_b64 s[12:13], s[12:13], 9
	global_load_dwordx2 v[60:61], v[26:27], off
	v_lshl_add_u64 v[26:27], v[4:5], 0, s[12:13]
	global_load_dwordx2 v[48:49], v[26:27], off
	v_lshl_add_u64 v[26:27], v[6:7], 0, s[12:13]
	v_readlane_b32 s12, v92, 12
	s_ashr_i32 s13, s12, 31
	s_lshl_b64 s[12:13], s[12:13], 9
	global_load_dwordx2 v[58:59], v[26:27], off
	v_lshl_add_u64 v[26:27], v[4:5], 0, s[12:13]
	global_load_dwordx2 v[46:47], v[26:27], off
	v_lshl_add_u64 v[26:27], v[6:7], 0, s[12:13]
	v_readlane_b32 s12, v92, 13
	s_ashr_i32 s13, s12, 31
	s_lshl_b64 s[12:13], s[12:13], 9
	global_load_dwordx2 v[56:57], v[26:27], off
	v_lshl_add_u64 v[26:27], v[4:5], 0, s[12:13]
	global_load_dwordx2 v[44:45], v[26:27], off
	v_lshl_add_u64 v[26:27], v[6:7], 0, s[12:13]
	v_readlane_b32 s12, v92, 14
	s_ashr_i32 s13, s12, 31
	s_lshl_b64 s[12:13], s[12:13], 9
	global_load_dwordx2 v[54:55], v[26:27], off
	v_lshl_add_u64 v[26:27], v[4:5], 0, s[12:13]
	global_load_dwordx2 v[42:43], v[26:27], off
	v_lshl_add_u64 v[26:27], v[6:7], 0, s[12:13]
	v_readlane_b32 s12, v92, 15
	s_ashr_i32 s13, s12, 31
	s_lshl_b64 s[12:13], s[12:13], 9
	global_load_dwordx2 v[52:53], v[26:27], off
	v_lshl_add_u64 v[26:27], v[4:5], 0, s[12:13]
	global_load_dwordx2 v[40:41], v[26:27], off
	v_lshl_add_u64 v[26:27], v[6:7], 0, s[12:13]
	global_load_dwordx2 v[36:37], v[26:27], off
	v_readlane_b32 s12, v253, 15
	v_readlane_b32 s13, v253, 16
	s_nop 1
	v_lshl_add_u64 v[26:27], s[12:13], 0, v[144:145]
	v_readlane_b32 s12, v253, 13
	v_lshlrev_b32_e32 v144, 6, v28
	v_readlane_b32 s13, v253, 14
	s_waitcnt lgkmcnt(0)
	v_lshl_add_u64 v[30:31], s[10:11], 0, v[144:145]
	v_readlane_b32 s10, v253, 23
	v_lshl_add_u64 v[28:29], s[12:13], 0, v[144:145]
	v_readlane_b32 s12, v253, 2
	v_readlane_b32 s13, v253, 3
	v_readlane_b32 s11, v253, 24
	v_readlane_b32 s14, v253, 4
	v_lshl_add_u64 v[32:33], s[12:13], 0, v[144:145]
	v_lshl_add_u64 v[34:35], s[10:11], 0, v[34:35]
	s_mov_b64 s[10:11], 0
	v_lshlrev_b32_e32 v144, 2, v2
	v_readlane_b32 s15, v253, 5
	global_load_dwordx4 v[124:127], v[30:31], off
	global_load_dwordx4 v[128:131], v[30:31], off offset:16
	global_load_dwordx4 v[132:135], v[30:31], off offset:32
	global_load_dwordx4 v[136:139], v[30:31], off offset:48
	v_readfirstlane_b32 s62, v4
	v_readfirstlane_b32 s63, v5
	v_readfirstlane_b32 s64, v6
	v_readfirstlane_b32 s65, v7
	v_and_b32_e32 v121, 63, v175
	v_lshlrev_b32_e32 v121, 3, v121

.LBB0_763:
	s_cmpk_eq_i32 s58, 0x80
	s_cselect_b64 s[12:13], -1, 0
	ds_bpermute_b32 v84, v93, v92
	s_and_b64 vcc, s[12:13], s[48:49]
	v_cndmask_b32_e32 v104, v0, v94, vcc
	v_ashrrev_i32_e32 v105, 31, v104
	s_and_b32 s12, s58, 0x70
	v_lshlrev_b64 v[104:105], 9, v[104:105]
	v_lshl_add_u64 v[104:105], s[94:95], 0, v[104:105]
	s_lshl_b32 s36, s12, 2
	s_waitcnt lgkmcnt(0)
	v_ashrrev_i32_e32 v85, 31, v84
	v_lshl_add_u64 v[104:105], v[104:105], 0, s[36:37]
	v_lshl_add_u64 v[84:85], v[84:85], 3, s[8:9]
	v_lshl_add_u64 v[104:105], v[104:105], 0, v[144:145]
	global_load_dwordx2 v[84:85], v[84:85], off
	s_nop 0
	global_load_dword v86, v[72:73], off
	global_load_dword v92, v[104:105], off
	s_waitcnt vmcnt(11)
	v_dot8_i32_i4 v87, v8, v1, 0
	v_dot8_i32_i4 v104, v8, v88, 0
	v_dot8_i32_i4 v87, v9, v89, v87
	v_dot8_i32_i4 v104, v9, v90, v104
	s_waitcnt vmcnt(10)
	v_dot8_i32_i4 v9, v10, v88, 0
	v_dot8_i32_i4 v9, v11, v90, v9
	v_lshl_add_u32 v8, v87, 4, v104
	v_cvt_f32_i32_e32 v87, v8
	v_dot8_i32_i4 v8, v10, v1, 0
	v_dot8_i32_i4 v8, v11, v89, v8
	s_add_i32 s58, s58, 16
	v_lshl_add_u64 v[72:73], v[72:73], 0, 64
	s_waitcnt vmcnt(2)
	v_mul_f32_e32 v85, v91, v85
	v_lshl_add_u32 v8, v8, 4, v9
	v_cvt_f32_i32_e32 v104, v8
	v_dot8_i32_i4 v8, v12, v1, 0
	v_dot8_i32_i4 v9, v12, v88, 0
	v_dot8_i32_i4 v8, v13, v89, v8
	v_dot8_i32_i4 v9, v13, v90, v9
	s_waitcnt vmcnt(0)
	v_readlane_b32 s12, v92, 0
	v_readlane_b32 s28, v92, 8
	v_readlane_b32 s30, v92, 9
	v_lshl_add_u32 v8, v8, 4, v9
	v_cvt_f32_i32_e32 v105, v8
	v_dot8_i32_i4 v8, v14, v1, 0
	v_dot8_i32_i4 v9, v14, v88, 0
	v_dot8_i32_i4 v8, v15, v89, v8
	v_dot8_i32_i4 v9, v15, v90, v9
	s_ashr_i32 s13, s12, 31
	v_readlane_b32 s14, v92, 1
	s_ashr_i32 s29, s28, 31
	v_lshl_add_u32 v8, v8, 4, v9
	v_cvt_f32_i32_e32 v106, v8
	v_dot8_i32_i4 v8, v16, v1, 0
	v_dot8_i32_i4 v9, v16, v88, 0
	v_dot8_i32_i4 v8, v17, v89, v8
	v_dot8_i32_i4 v9, v17, v90, v9
	s_ashr_i32 s31, s30, 31
	v_readlane_b32 s34, v92, 10
	s_lshl_b64 s[12:13], s[12:13], 9
	v_lshl_add_u32 v8, v8, 4, v9
	v_cvt_f32_i32_e32 v107, v8
	v_dot8_i32_i4 v8, v18, v1, 0
	v_dot8_i32_i4 v9, v18, v88, 0
	v_dot8_i32_i4 v8, v19, v89, v8
	v_dot8_i32_i4 v9, v19, v90, v9
	s_ashr_i32 s15, s14, 31
	v_readlane_b32 s16, v92, 2
	s_lshl_b64 s[28:29], s[28:29], 9
	v_lshl_add_u32 v8, v8, 4, v9
	v_cvt_f32_i32_e32 v108, v8
	v_dot8_i32_i4 v8, v20, v1, 0
	v_dot8_i32_i4 v9, v20, v88, 0
	v_dot8_i32_i4 v8, v21, v89, v8
	v_dot8_i32_i4 v9, v21, v90, v9
	s_lshl_b64 s[30:31], s[30:31], 9
	s_ashr_i32 s35, s34, 31
	v_readlane_b32 s38, v92, 11
	v_lshl_add_u32 v8, v8, 4, v9
	v_cvt_f32_i32_e32 v109, v8
	v_dot8_i32_i4 v8, v22, v1, 0
	v_dot8_i32_i4 v9, v22, v88, 0
	v_dot8_i32_i4 v8, v23, v89, v8
	v_dot8_i32_i4 v9, v23, v90, v9
	s_lshl_b64 s[14:15], s[14:15], 9
	s_ashr_i32 s17, s16, 31
	v_readlane_b32 s18, v92, 3
	v_lshl_add_u32 v8, v8, 4, v9
	v_cvt_f32_i32_e32 v110, v8
	v_dot8_i32_i4 v8, v24, v1, 0
	v_dot8_i32_i4 v9, v24, v88, 0
	v_dot8_i32_i4 v8, v25, v89, v8
	v_dot8_i32_i4 v9, v25, v90, v9
	s_lshl_b64 s[34:35], s[34:35], 9
	s_ashr_i32 s39, s38, 31
	s_nop 0
	v_lshl_add_u32 v8, v8, 4, v9
	v_cvt_f32_i32_e32 v111, v8
	v_dot8_i32_i4 v8, v38, v1, 0
	v_dot8_i32_i4 v9, v38, v88, 0
	v_dot8_i32_i4 v8, v39, v89, v8
	v_dot8_i32_i4 v9, v39, v90, v9
	v_permlane32_swap_b32 v87, v111
	s_nop 1
	v_lshl_add_u32 v8, v8, 4, v9
	v_cvt_f32_i32_e32 v112, v8
	v_dot8_i32_i4 v8, v50, v1, 0
	v_dot8_i32_i4 v9, v50, v88, 0
	v_dot8_i32_i4 v8, v51, v89, v8
	v_dot8_i32_i4 v9, v51, v90, v9
	s_waitcnt lgkmcnt(0)
	v_add_f32_e32 v87, v87, v111
	v_permlane32_swap_b32 v104, v112
	v_lshl_add_u32 v8, v8, 4, v9
	v_cvt_f32_i32_e32 v113, v8
	v_dot8_i32_i4 v8, v48, v1, 0
	v_dot8_i32_i4 v9, v48, v88, 0
	v_dot8_i32_i4 v8, v49, v89, v8
	v_dot8_i32_i4 v9, v49, v90, v9
	s_waitcnt lgkmcnt(0)
	v_add_f32_e32 v104, v104, v112
	v_permlane32_swap_b32 v105, v113
	v_lshl_add_u32 v8, v8, 4, v9
	v_cvt_f32_i32_e32 v114, v8
	v_dot8_i32_i4 v8, v46, v1, 0
	v_dot8_i32_i4 v9, v46, v88, 0
	v_dot8_i32_i4 v8, v47, v89, v8
	v_dot8_i32_i4 v9, v47, v90, v9
	s_waitcnt lgkmcnt(0)
	v_add_f32_e32 v105, v105, v113
	v_permlane32_swap_b32 v106, v114
	v_lshl_add_u32 v8, v8, 4, v9
	v_cvt_f32_i32_e32 v115, v8
	v_dot8_i32_i4 v8, v44, v1, 0
	v_dot8_i32_i4 v9, v44, v88, 0
	v_dot8_i32_i4 v8, v45, v89, v8
	v_dot8_i32_i4 v9, v45, v90, v9
	s_waitcnt lgkmcnt(0)
	v_add_f32_e32 v106, v106, v114
	v_permlane32_swap_b32 v107, v115
	v_lshl_add_u32 v8, v8, 4, v9
	v_cvt_f32_i32_e32 v116, v8
	v_dot8_i32_i4 v8, v42, v1, 0
	v_dot8_i32_i4 v9, v42, v88, 0
	v_dot8_i32_i4 v8, v43, v89, v8
	v_dot8_i32_i4 v9, v43, v90, v9
	s_waitcnt lgkmcnt(0)
	v_add_f32_e32 v107, v107, v115
	v_permlane32_swap_b32 v108, v116
	v_lshl_add_u32 v8, v8, 4, v9
	v_cvt_f32_i32_e32 v117, v8
	v_dot8_i32_i4 v8, v40, v1, 0
	v_dot8_i32_i4 v9, v40, v88, 0
	v_dot8_i32_i4 v8, v41, v89, v8
	v_dot8_i32_i4 v9, v41, v90, v9
	s_waitcnt lgkmcnt(0)
	v_add_f32_e32 v108, v108, v116
	v_permlane32_swap_b32 v109, v117
	v_lshl_add_u32 v8, v8, 4, v9
	v_cvt_f32_i32_e32 v118, v8
	s_waitcnt lgkmcnt(0)
	v_add_f32_e32 v109, v109, v117
	v_permlane32_swap_b32 v110, v118
	v_readlane_b32 s50, v92, 12
	s_lshl_b64 s[16:17], s[16:17], 9
	s_ashr_i32 s19, s18, 31
	s_waitcnt lgkmcnt(0)
	v_add_f32_e32 v110, v110, v118
	v_permlane16_swap_b32 v87, v107
	v_readlane_b32 s20, v92, 4
	s_add_u32 s66, s28, s62
	s_addc_u32 s67, s29, s63
	global_load_dwordx2 v[24:25], v121, s[66:67]
	s_add_u32 s66, s30, s62
	s_addc_u32 s67, s31, s63
	global_load_dwordx2 v[38:39], v121, s[66:67]
	s_waitcnt lgkmcnt(0)
	v_add_f32_e32 v87, v87, v107
	v_permlane16_swap_b32 v104, v108
	s_lshl_b64 s[38:39], s[38:39], 9
	s_ashr_i32 s51, s50, 31
	v_readlane_b32 s52, v92, 13
	s_waitcnt lgkmcnt(0)
	v_add_f32_e32 v104, v104, v108
	v_permlane16_swap_b32 v105, v109
	s_lshl_b64 s[18:19], s[18:19], 9
	s_ashr_i32 s21, s20, 31
	v_readlane_b32 s22, v92, 5
	s_waitcnt lgkmcnt(0)
	v_add_f32_e32 v105, v105, v109
	v_permlane16_swap_b32 v106, v110
	s_add_u32 s66, s34, s62
	s_addc_u32 s67, s35, s63
	global_load_dwordx2 v[50:51], v121, s[66:67]
	s_lshl_b64 s[50:51], s[50:51], 9
	s_ashr_i32 s53, s52, 31
	s_waitcnt lgkmcnt(0)
	v_add_f32_e32 v106, v106, v110
	v_cndmask_b32_e64 v107, v87, v105, s[44:45]
	v_cndmask_b32_e64 v87, v105, v87, s[44:45]
	s_nop 0
	v_mov_b32_dpp v105, v107 row_ror:8 row_mask:0xf bank_mask:0xf
	v_readlane_b32 s54, v92, 14
	s_lshl_b64 s[20:21], s[20:21], 9
	s_ashr_i32 s23, s22, 31
	v_readlane_b32 s24, v92, 6
	s_waitcnt lgkmcnt(0)
	v_add_f32_e32 v87, v87, v105
	v_cndmask_b32_e64 v105, v104, v106, s[44:45]
	s_nop 1
	v_mov_b32_dpp v105, v105 row_ror:8 row_mask:0xf bank_mask:0xf
	v_cndmask_b32_e64 v104, v106, v104, s[44:45]
	s_lshl_b64 s[52:53], s[52:53], 9
	s_ashr_i32 s55, s54, 31
	v_readlane_b32 s56, v92, 15
	s_waitcnt lgkmcnt(0)
	v_add_f32_e32 v104, v104, v105
	v_cndmask_b32_e64 v105, v87, v104, s[46:47]
	v_cndmask_b32_e64 v87, v104, v87, s[46:47]
	s_nop 0
	v_mov_b32_dpp v104, v105 row_half_mirror row_mask:0xf bank_mask:0xf
	s_nop 1
	v_mov_b32_dpp v104, v104 quad_perm:[3,2,1,0] row_mask:0xf bank_mask:0xf
	s_lshl_b64 s[22:23], s[22:23], 9
	s_ashr_i32 s25, s24, 31
	v_readlane_b32 s26, v92, 7
	s_lshl_b64 s[54:55], s[54:55], 9
	s_waitcnt lgkmcnt(0)
	v_add_f32_e32 v87, v87, v104
	s_nop 1
	v_mov_b32_dpp v104, v87 quad_perm:[2,3,0,1] row_mask:0xf bank_mask:0xf
	s_ashr_i32 s57, s56, 31
	s_lshl_b64 s[24:25], s[24:25], 9
	s_ashr_i32 s27, s26, 31
	s_lshl_b64 s[56:57], s[56:57], 9
	s_waitcnt lgkmcnt(0)
	v_add_f32_e32 v87, v87, v104
	s_nop 1
	v_mov_b32_dpp v104, v87 quad_perm:[1,0,3,2] row_mask:0xf bank_mask:0xf
	s_lshl_b64 s[26:27], s[26:27], 9
	s_waitcnt lgkmcnt(0)
	v_add_f32_e32 v87, v87, v104
	v_add_f32_e32 v87, v95, v87
	v_mul_f32_e32 v85, v85, v87
	v_mul_f32_e32 v87, 0x3d372713, v85
	v_mul_f32_e32 v87, v85, v87
	v_fma_f32 v87, v85, v87, v85
	v_mul_f32_e32 v87, 0x3fcc422a, v87
	v_mul_f32_e32 v87, 0xbfb8aa3b, v87
	v_exp_f32_e32 v87, v87
	v_lshlrev_b32_e32 v104, 4, v82
	v_add_f32_e32 v87, 1.0, v87
	v_rcp_f32_e32 v87, v87
	s_nop 0
	v_pk_mul_f32 v[84:85], v[84:85], v[86:87]
	v_lshrrev_b32_e32 v87, 4, v82
	v_pk_mul_f32 v[84:85], v[84:85], v[84:85] op_sel:[0,1] op_sel_hi:[1,0]
	v_cvt_f16_f32_e32 v120, v84
	v_and_b32_e32 v86, 0x7070707, v82
	v_readlane_b32 s36, v120, 0
	v_and_b32_e32 v87, 0x7070707, v87
	v_perm_b32 v86, s2, v205, v86
	v_perm_b32 v87, s2, v205, v87
	v_and_or_b32 v86, v104, s4, v86
	v_and_or_b32 v82, v82, s4, v87
	v_perm_b32 v87, v82, v86, s5
	v_perm_b32 v104, v82, v86, s33
	v_perm_b32 v105, v82, v86, s0
	v_perm_b32 v82, v82, v86, s1
	v_pk_fma_f16 v86, v87, s36, v103 op_sel_hi:[1,0,1]
	v_pk_fma_f16 v87, v104, s36, v102 op_sel_hi:[1,0,1]
	v_lshrrev_b32_e32 v102, 4, v83
	v_pk_fma_f16 v82, v82, s36, v100 op_sel_hi:[1,0,1]
	v_and_b32_e32 v100, 0x7070707, v83
	v_and_b32_e32 v102, 0x7070707, v102
	v_perm_b32 v100, s2, v205, v100
	v_perm_b32 v102, s2, v205, v102
	v_lshlrev_b32_e32 v103, 4, v83
	v_and_or_b32 v100, v103, s4, v100
	v_and_or_b32 v83, v83, s4, v102
	v_perm_b32 v102, v83, v100, s5
	v_perm_b32 v103, v83, v100, s33
	v_perm_b32 v104, v83, v100, s0
	v_perm_b32 v83, v83, v100, s1
	v_readlane_b32 s59, v120, 4
	v_lshrrev_b32_e32 v100, 4, v80
	v_pk_fma_f16 v101, v105, s36, v101 op_sel_hi:[1,0,1]
	v_pk_fma_f16 v99, v102, s36, v99 op_sel_hi:[1,0,1]
	v_pk_fma_f16 v98, v103, s36, v98 op_sel_hi:[1,0,1]
	v_pk_fma_f16 v97, v104, s36, v97 op_sel_hi:[1,0,1]
	v_pk_fma_f16 v83, v83, s36, v96 op_sel_hi:[1,0,1]
	v_and_b32_e32 v96, 0x7070707, v80
	v_and_b32_e32 v100, 0x7070707, v100
	v_perm_b32 v96, s2, v205, v96
	v_perm_b32 v100, s2, v205, v100
	v_lshlrev_b32_e32 v102, 4, v80
	v_and_or_b32 v96, v102, s4, v96
	v_and_or_b32 v80, v80, s4, v100
	v_perm_b32 v100, v80, v96, s5
	v_perm_b32 v102, v80, v96, s33
	v_perm_b32 v103, v80, v96, s0
	v_perm_b32 v80, v80, v96, s1
	v_pk_fma_f16 v86, v100, s59, v86 op_sel_hi:[1,0,1]
	v_lshrrev_b32_e32 v100, 4, v81
	v_pk_fma_f16 v80, v80, s59, v82 op_sel_hi:[1,0,1]
	v_and_b32_e32 v82, 0x7070707, v81
	v_and_b32_e32 v100, 0x7070707, v100
	v_pk_fma_f16 v96, v103, s59, v101 op_sel_hi:[1,0,1]
	v_perm_b32 v82, s2, v205, v82
	v_perm_b32 v100, s2, v205, v100
	v_lshlrev_b32_e32 v101, 4, v81
	v_and_or_b32 v82, v101, s4, v82
	v_and_or_b32 v81, v81, s4, v100
	v_perm_b32 v100, v81, v82, s5
	v_pk_fma_f16 v87, v102, s59, v87 op_sel_hi:[1,0,1]
	v_perm_b32 v101, v81, v82, s33
	v_perm_b32 v102, v81, v82, s0
	v_perm_b32 v81, v81, v82, s1
	v_pk_fma_f16 v82, v100, s59, v99 op_sel_hi:[1,0,1]
	v_readlane_b32 s60, v120, 8
	v_lshrrev_b32_e32 v99, 4, v78
	v_pk_fma_f16 v98, v101, s59, v98 op_sel_hi:[1,0,1]
	v_pk_fma_f16 v97, v102, s59, v97 op_sel_hi:[1,0,1]
	v_pk_fma_f16 v81, v81, s59, v83 op_sel_hi:[1,0,1]
	v_and_b32_e32 v85, 0x7070707, v78
	v_and_b32_e32 v99, 0x7070707, v99
	v_perm_b32 v85, s2, v205, v85
	v_perm_b32 v99, s2, v205, v99
	v_lshlrev_b32_e32 v100, 4, v78
	v_and_or_b32 v85, v100, s4, v85
	v_and_or_b32 v78, v78, s4, v99
	v_perm_b32 v99, v78, v85, s5
	v_perm_b32 v100, v78, v85, s33
	v_perm_b32 v101, v78, v85, s0
	v_perm_b32 v78, v78, v85, s1
	v_pk_fma_f16 v85, v99, s60, v86 op_sel_hi:[1,0,1]
	v_pk_fma_f16 v86, v100, s60, v87 op_sel_hi:[1,0,1]
	v_pk_fma_f16 v87, v101, s60, v96 op_sel_hi:[1,0,1]
	v_lshrrev_b32_e32 v96, 4, v79
	v_pk_fma_f16 v78, v78, s60, v80 op_sel_hi:[1,0,1]
	v_and_b32_e32 v80, 0x7070707, v79
	v_and_b32_e32 v96, 0x7070707, v96
	v_perm_b32 v80, s2, v205, v80
	v_perm_b32 v96, s2, v205, v96
	v_lshlrev_b32_e32 v99, 4, v79
	v_and_or_b32 v80, v99, s4, v80
	v_and_or_b32 v79, v79, s4, v96
	v_perm_b32 v96, v79, v80, s5
	v_perm_b32 v100, v79, v80, s0
	v_perm_b32 v99, v79, v80, s33
	v_perm_b32 v79, v79, v80, s1
	v_pk_fma_f16 v80, v96, s60, v82 op_sel_hi:[1,0,1]
	v_pk_fma_f16 v96, v100, s60, v97 op_sel_hi:[1,0,1]
	v_readlane_b32 s36, v120, 12
	v_lshrrev_b32_e32 v97, 4, v76
	v_pk_fma_f16 v82, v99, s60, v98 op_sel_hi:[1,0,1]
	v_pk_fma_f16 v79, v79, s60, v81 op_sel_hi:[1,0,1]
	v_and_b32_e32 v83, 0x7070707, v76
	v_and_b32_e32 v97, 0x7070707, v97
	v_perm_b32 v83, s2, v205, v83
	v_perm_b32 v97, s2, v205, v97
	v_lshlrev_b32_e32 v98, 4, v76
	v_and_or_b32 v83, v98, s4, v83
	v_and_or_b32 v76, v76, s4, v97
	v_perm_b32 v97, v76, v83, s5
	v_perm_b32 v98, v76, v83, s33
	v_perm_b32 v99, v76, v83, s0
	v_perm_b32 v76, v76, v83, s1
	v_pk_fma_f16 v83, v97, s36, v85 op_sel_hi:[1,0,1]
	v_pk_fma_f16 v85, v98, s36, v86 op_sel_hi:[1,0,1]
	v_pk_fma_f16 v86, v99, s36, v87 op_sel_hi:[1,0,1]
	v_lshrrev_b32_e32 v87, 4, v77
	v_pk_fma_f16 v76, v76, s36, v78 op_sel_hi:[1,0,1]
	v_and_b32_e32 v78, 0x7070707, v77
	v_and_b32_e32 v87, 0x7070707, v87
	v_perm_b32 v78, s2, v205, v78
	v_perm_b32 v87, s2, v205, v87
	v_lshlrev_b32_e32 v97, 4, v77
	v_and_or_b32 v78, v97, s4, v78
	v_and_or_b32 v77, v77, s4, v87
	v_perm_b32 v87, v77, v78, s5
	v_perm_b32 v97, v77, v78, s33
	v_perm_b32 v98, v77, v78, s0
	v_perm_b32 v77, v77, v78, s1
	v_pk_fma_f16 v78, v87, s36, v80 op_sel_hi:[1,0,1]
	v_readlane_b32 s59, v120, 16
	v_lshrrev_b32_e32 v87, 4, v74
	v_pk_fma_f16 v80, v97, s36, v82 op_sel_hi:[1,0,1]
	v_pk_fma_f16 v82, v98, s36, v96 op_sel_hi:[1,0,1]
	v_pk_fma_f16 v77, v77, s36, v79 op_sel_hi:[1,0,1]
	v_and_b32_e32 v81, 0x7070707, v74
	v_and_b32_e32 v87, 0x7070707, v87
	v_perm_b32 v81, s2, v205, v81
	v_perm_b32 v87, s2, v205, v87
	v_lshlrev_b32_e32 v96, 4, v74
	v_and_or_b32 v81, v96, s4, v81
	v_and_or_b32 v74, v74, s4, v87
	v_perm_b32 v87, v74, v81, s5
	v_perm_b32 v96, v74, v81, s33
	v_perm_b32 v97, v74, v81, s0
	v_perm_b32 v74, v74, v81, s1
	v_pk_fma_f16 v81, v87, s59, v83 op_sel_hi:[1,0,1]
	v_pk_fma_f16 v83, v96, s59, v85 op_sel_hi:[1,0,1]
	v_pk_fma_f16 v85, v97, s59, v86 op_sel_hi:[1,0,1]
	v_lshrrev_b32_e32 v86, 4, v75
	v_pk_fma_f16 v74, v74, s59, v76 op_sel_hi:[1,0,1]
	v_and_b32_e32 v76, 0x7070707, v75
	v_and_b32_e32 v86, 0x7070707, v86
	v_perm_b32 v76, s2, v205, v76
	v_perm_b32 v86, s2, v205, v86
	v_lshlrev_b32_e32 v87, 4, v75
	v_and_or_b32 v76, v87, s4, v76
	v_and_or_b32 v75, v75, s4, v86
	v_perm_b32 v86, v75, v76, s5
	v_perm_b32 v87, v75, v76, s33
	v_perm_b32 v96, v75, v76, s0
	v_perm_b32 v75, v75, v76, s1
	v_pk_fma_f16 v76, v86, s59, v78 op_sel_hi:[1,0,1]
	v_pk_fma_f16 v78, v87, s59, v80 op_sel_hi:[1,0,1]
	v_pk_fma_f16 v80, v96, s59, v82 op_sel_hi:[1,0,1]
	v_readlane_b32 s60, v120, 20
	v_lshrrev_b32_e32 v82, 4, v70
	v_pk_fma_f16 v75, v75, s59, v77 op_sel_hi:[1,0,1]
	v_and_b32_e32 v79, 0x7070707, v70
	v_and_b32_e32 v82, 0x7070707, v82
	v_perm_b32 v79, s2, v205, v79
	v_perm_b32 v82, s2, v205, v82
	v_lshlrev_b32_e32 v86, 4, v70
	v_and_or_b32 v79, v86, s4, v79
	v_and_or_b32 v70, v70, s4, v82
	v_perm_b32 v82, v70, v79, s5
	v_perm_b32 v86, v70, v79, s33
	v_perm_b32 v87, v70, v79, s0
	v_perm_b32 v70, v70, v79, s1
	v_pk_fma_f16 v79, v82, s60, v81 op_sel_hi:[1,0,1]
	v_pk_fma_f16 v81, v86, s60, v83 op_sel_hi:[1,0,1]
	v_lshrrev_b32_e32 v83, 4, v71
	v_pk_fma_f16 v70, v70, s60, v74 op_sel_hi:[1,0,1]
	v_and_b32_e32 v74, 0x7070707, v71
	v_and_b32_e32 v83, 0x7070707, v83
	v_pk_fma_f16 v82, v87, s60, v85 op_sel_hi:[1,0,1]
	v_perm_b32 v74, s2, v205, v74
	v_perm_b32 v83, s2, v205, v83
	v_lshlrev_b32_e32 v85, 4, v71
	v_and_or_b32 v74, v85, s4, v74
	v_and_or_b32 v71, v71, s4, v83
	v_perm_b32 v83, v71, v74, s5
	v_perm_b32 v85, v71, v74, s33
	v_perm_b32 v86, v71, v74, s0
	v_perm_b32 v71, v71, v74, s1
	v_pk_fma_f16 v74, v83, s60, v76 op_sel_hi:[1,0,1]
	v_pk_fma_f16 v76, v85, s60, v78 op_sel_hi:[1,0,1]
	v_pk_fma_f16 v78, v86, s60, v80 op_sel_hi:[1,0,1]
	v_readlane_b32 s36, v120, 24
	v_lshrrev_b32_e32 v80, 4, v68
	v_pk_fma_f16 v71, v71, s60, v75 op_sel_hi:[1,0,1]
	v_and_b32_e32 v77, 0x7070707, v68
	v_and_b32_e32 v80, 0x7070707, v80
	v_perm_b32 v77, s2, v205, v77
	v_perm_b32 v80, s2, v205, v80
	v_lshlrev_b32_e32 v83, 4, v68
	v_and_or_b32 v77, v83, s4, v77
	v_and_or_b32 v68, v68, s4, v80
	v_perm_b32 v80, v68, v77, s5
	v_perm_b32 v83, v68, v77, s33
	v_perm_b32 v85, v68, v77, s0
	v_perm_b32 v68, v68, v77, s1
	v_pk_fma_f16 v77, v80, s36, v79 op_sel_hi:[1,0,1]
	v_pk_fma_f16 v79, v83, s36, v81 op_sel_hi:[1,0,1]
	v_lshrrev_b32_e32 v81, 4, v69
	v_pk_fma_f16 v68, v68, s36, v70 op_sel_hi:[1,0,1]
	v_and_b32_e32 v70, 0x7070707, v69
	v_and_b32_e32 v81, 0x7070707, v81
	v_pk_fma_f16 v80, v85, s36, v82 op_sel_hi:[1,0,1]
	v_perm_b32 v70, s2, v205, v70
	v_perm_b32 v81, s2, v205, v81
	v_lshlrev_b32_e32 v82, 4, v69
	v_and_or_b32 v70, v82, s4, v70
	v_and_or_b32 v69, v69, s4, v81
	v_perm_b32 v81, v69, v70, s5
	v_perm_b32 v82, v69, v70, s33
	v_perm_b32 v83, v69, v70, s0
	v_perm_b32 v69, v69, v70, s1
	v_pk_fma_f16 v70, v81, s36, v74 op_sel_hi:[1,0,1]
	v_pk_fma_f16 v74, v82, s36, v76 op_sel_hi:[1,0,1]
	v_pk_fma_f16 v76, v83, s36, v78 op_sel_hi:[1,0,1]
	v_readlane_b32 s59, v120, 28
	v_lshrrev_b32_e32 v78, 4, v64
	v_pk_fma_f16 v69, v69, s36, v71 op_sel_hi:[1,0,1]
	v_and_b32_e32 v75, 0x7070707, v64
	v_and_b32_e32 v78, 0x7070707, v78
	v_perm_b32 v75, s2, v205, v75
	v_perm_b32 v78, s2, v205, v78
	v_lshlrev_b32_e32 v81, 4, v64
	v_and_or_b32 v75, v81, s4, v75
	v_and_or_b32 v64, v64, s4, v78
	v_perm_b32 v78, v64, v75, s5
	v_perm_b32 v81, v64, v75, s33
	v_perm_b32 v82, v64, v75, s0
	v_perm_b32 v64, v64, v75, s1
	v_pk_fma_f16 v75, v78, s59, v77 op_sel_hi:[1,0,1]
	v_pk_fma_f16 v77, v81, s59, v79 op_sel_hi:[1,0,1]
	v_lshrrev_b32_e32 v79, 4, v65
	v_pk_fma_f16 v64, v64, s59, v68 op_sel_hi:[1,0,1]
	v_and_b32_e32 v68, 0x7070707, v65
	v_and_b32_e32 v79, 0x7070707, v79
	v_pk_fma_f16 v78, v82, s59, v80 op_sel_hi:[1,0,1]
	v_perm_b32 v68, s2, v205, v68
	v_perm_b32 v79, s2, v205, v79
	v_lshlrev_b32_e32 v80, 4, v65
	v_and_or_b32 v68, v80, s4, v68
	v_and_or_b32 v65, v65, s4, v79
	v_perm_b32 v79, v65, v68, s5
	v_perm_b32 v80, v65, v68, s33
	v_perm_b32 v81, v65, v68, s0
	v_perm_b32 v65, v65, v68, s1
	v_pk_fma_f16 v68, v79, s59, v70 op_sel_hi:[1,0,1]
	v_pk_fma_f16 v70, v80, s59, v74 op_sel_hi:[1,0,1]
	v_pk_fma_f16 v74, v81, s59, v76 op_sel_hi:[1,0,1]
	v_readlane_b32 s60, v120, 32
	v_lshrrev_b32_e32 v76, 4, v62
	v_pk_fma_f16 v65, v65, s59, v69 op_sel_hi:[1,0,1]
	v_and_b32_e32 v71, 0x7070707, v62
	v_and_b32_e32 v76, 0x7070707, v76
	v_perm_b32 v71, s2, v205, v71
	v_perm_b32 v76, s2, v205, v76
	v_lshlrev_b32_e32 v79, 4, v62
	v_and_or_b32 v71, v79, s4, v71
	v_and_or_b32 v62, v62, s4, v76
	v_perm_b32 v76, v62, v71, s5
	v_perm_b32 v79, v62, v71, s33
	v_perm_b32 v80, v62, v71, s0
	v_perm_b32 v62, v62, v71, s1
	v_pk_fma_f16 v71, v76, s60, v75 op_sel_hi:[1,0,1]
	v_pk_fma_f16 v75, v79, s60, v77 op_sel_hi:[1,0,1]
	v_lshrrev_b32_e32 v77, 4, v63
	v_pk_fma_f16 v62, v62, s60, v64 op_sel_hi:[1,0,1]
	v_and_b32_e32 v64, 0x7070707, v63
	v_and_b32_e32 v77, 0x7070707, v77
	v_pk_fma_f16 v76, v80, s60, v78 op_sel_hi:[1,0,1]
	v_perm_b32 v64, s2, v205, v64
	v_perm_b32 v77, s2, v205, v77
	v_lshlrev_b32_e32 v78, 4, v63
	v_and_or_b32 v64, v78, s4, v64
	v_and_or_b32 v63, v63, s4, v77
	v_perm_b32 v77, v63, v64, s5
	v_perm_b32 v78, v63, v64, s33
	v_perm_b32 v79, v63, v64, s0
	v_perm_b32 v63, v63, v64, s1
	v_pk_fma_f16 v64, v77, s60, v68 op_sel_hi:[1,0,1]
	v_pk_fma_f16 v68, v78, s60, v70 op_sel_hi:[1,0,1]
	v_pk_fma_f16 v70, v79, s60, v74 op_sel_hi:[1,0,1]
	v_readlane_b32 s36, v120, 36
	v_lshrrev_b32_e32 v74, 4, v66
	v_pk_fma_f16 v63, v63, s60, v65 op_sel_hi:[1,0,1]
	v_and_b32_e32 v69, 0x7070707, v66
	v_and_b32_e32 v74, 0x7070707, v74
	v_perm_b32 v69, s2, v205, v69
	v_perm_b32 v74, s2, v205, v74
	v_lshlrev_b32_e32 v77, 4, v66
	v_and_or_b32 v69, v77, s4, v69
	v_and_or_b32 v66, v66, s4, v74
	v_perm_b32 v74, v66, v69, s5
	v_perm_b32 v77, v66, v69, s33
	v_perm_b32 v78, v66, v69, s0
	v_perm_b32 v66, v66, v69, s1
	v_pk_fma_f16 v69, v74, s36, v71 op_sel_hi:[1,0,1]
	v_pk_fma_f16 v71, v77, s36, v75 op_sel_hi:[1,0,1]
	v_lshrrev_b32_e32 v75, 4, v67
	v_pk_fma_f16 v62, v66, s36, v62 op_sel_hi:[1,0,1]
	v_and_b32_e32 v66, 0x7070707, v67
	v_and_b32_e32 v75, 0x7070707, v75
	v_pk_fma_f16 v74, v78, s36, v76 op_sel_hi:[1,0,1]
	v_perm_b32 v66, s2, v205, v66
	v_perm_b32 v75, s2, v205, v75
	v_lshlrev_b32_e32 v76, 4, v67
	v_and_or_b32 v66, v76, s4, v66
	v_and_or_b32 v67, v67, s4, v75
	v_perm_b32 v76, v67, v66, s33
	v_perm_b32 v77, v67, v66, s0
	v_perm_b32 v75, v67, v66, s5
	v_perm_b32 v66, v67, v66, s1
	v_pk_fma_f16 v67, v76, s36, v68 op_sel_hi:[1,0,1]
	v_pk_fma_f16 v68, v77, s36, v70 op_sel_hi:[1,0,1]
	v_readlane_b32 s59, v120, 40
	v_lshrrev_b32_e32 v70, 4, v60
	v_pk_fma_f16 v64, v75, s36, v64 op_sel_hi:[1,0,1]
	v_pk_fma_f16 v63, v66, s36, v63 op_sel_hi:[1,0,1]
	v_and_b32_e32 v66, 0x7070707, v60
	v_and_b32_e32 v70, 0x7070707, v70
	v_perm_b32 v66, s2, v205, v66
	v_perm_b32 v70, s2, v205, v70
	v_lshlrev_b32_e32 v75, 4, v60
	v_and_or_b32 v66, v75, s4, v66
	v_and_or_b32 v60, v60, s4, v70
	v_perm_b32 v70, v60, v66, s5
	v_perm_b32 v75, v60, v66, s33
	v_perm_b32 v76, v60, v66, s0
	v_perm_b32 v60, v60, v66, s1
	v_pk_fma_f16 v66, v70, s59, v69 op_sel_hi:[1,0,1]
	v_pk_fma_f16 v69, v75, s59, v71 op_sel_hi:[1,0,1]
	v_lshrrev_b32_e32 v71, 4, v61
	v_pk_fma_f16 v60, v60, s59, v62 op_sel_hi:[1,0,1]
	v_and_b32_e32 v62, 0x7070707, v61
	v_and_b32_e32 v71, 0x7070707, v71
	v_pk_fma_f16 v70, v76, s59, v74 op_sel_hi:[1,0,1]
	v_perm_b32 v62, s2, v205, v62
	v_perm_b32 v71, s2, v205, v71
	v_lshlrev_b32_e32 v74, 4, v61
	v_and_or_b32 v62, v74, s4, v62
	v_and_or_b32 v61, v61, s4, v71
	v_perm_b32 v71, v61, v62, s5
	v_perm_b32 v74, v61, v62, s33
	v_perm_b32 v75, v61, v62, s0
	v_perm_b32 v61, v61, v62, s1
	v_pk_fma_f16 v62, v71, s59, v64 op_sel_hi:[1,0,1]
	v_pk_fma_f16 v64, v74, s59, v67 op_sel_hi:[1,0,1]
	v_pk_fma_f16 v67, v75, s59, v68 op_sel_hi:[1,0,1]
	v_readlane_b32 s60, v120, 44
	v_lshrrev_b32_e32 v68, 4, v58
	v_pk_fma_f16 v61, v61, s59, v63 op_sel_hi:[1,0,1]
	v_and_b32_e32 v65, 0x7070707, v58
	v_and_b32_e32 v68, 0x7070707, v68
	v_perm_b32 v65, s2, v205, v65
	v_perm_b32 v68, s2, v205, v68
	v_lshlrev_b32_e32 v71, 4, v58
	v_and_or_b32 v65, v71, s4, v65
	v_and_or_b32 v58, v58, s4, v68
	v_perm_b32 v68, v58, v65, s5
	v_perm_b32 v71, v58, v65, s33
	v_perm_b32 v74, v58, v65, s0
	v_perm_b32 v58, v58, v65, s1
	v_pk_fma_f16 v65, v68, s60, v66 op_sel_hi:[1,0,1]
	v_pk_fma_f16 v66, v71, s60, v69 op_sel_hi:[1,0,1]
	v_lshrrev_b32_e32 v69, 4, v59
	v_pk_fma_f16 v58, v58, s60, v60 op_sel_hi:[1,0,1]
	v_and_b32_e32 v60, 0x7070707, v59
	v_and_b32_e32 v69, 0x7070707, v69
	v_pk_fma_f16 v68, v74, s60, v70 op_sel_hi:[1,0,1]
	v_perm_b32 v60, s2, v205, v60
	v_perm_b32 v69, s2, v205, v69
	v_lshlrev_b32_e32 v70, 4, v59
	v_and_or_b32 v60, v70, s4, v60
	v_and_or_b32 v59, v59, s4, v69
	v_perm_b32 v69, v59, v60, s5
	v_perm_b32 v70, v59, v60, s33
	v_perm_b32 v71, v59, v60, s0
	v_perm_b32 v59, v59, v60, s1
	v_pk_fma_f16 v60, v69, s60, v62 op_sel_hi:[1,0,1]
	v_pk_fma_f16 v62, v70, s60, v64 op_sel_hi:[1,0,1]
	v_pk_fma_f16 v64, v71, s60, v67 op_sel_hi:[1,0,1]
	v_readlane_b32 s36, v120, 48
	v_lshrrev_b32_e32 v67, 4, v56
	v_pk_fma_f16 v59, v59, s60, v61 op_sel_hi:[1,0,1]
	v_and_b32_e32 v63, 0x7070707, v56
	v_and_b32_e32 v67, 0x7070707, v67
	v_perm_b32 v63, s2, v205, v63
	v_perm_b32 v67, s2, v205, v67
	v_lshlrev_b32_e32 v69, 4, v56
	v_and_or_b32 v63, v69, s4, v63
	v_and_or_b32 v56, v56, s4, v67
	v_perm_b32 v67, v56, v63, s5
	v_perm_b32 v69, v56, v63, s33
	v_perm_b32 v70, v56, v63, s0
	v_perm_b32 v56, v56, v63, s1
	v_pk_fma_f16 v63, v67, s36, v65 op_sel_hi:[1,0,1]
	v_lshrrev_b32_e32 v67, 4, v57
	v_pk_fma_f16 v56, v56, s36, v58 op_sel_hi:[1,0,1]
	v_and_b32_e32 v58, 0x7070707, v57
	v_and_b32_e32 v67, 0x7070707, v67
	v_pk_fma_f16 v65, v69, s36, v66 op_sel_hi:[1,0,1]
	v_pk_fma_f16 v66, v70, s36, v68 op_sel_hi:[1,0,1]
	v_perm_b32 v58, s2, v205, v58
	v_perm_b32 v67, s2, v205, v67
	v_lshlrev_b32_e32 v68, 4, v57
	v_and_or_b32 v58, v68, s4, v58
	v_and_or_b32 v57, v57, s4, v67
	v_perm_b32 v67, v57, v58, s5
	v_perm_b32 v68, v57, v58, s33
	v_perm_b32 v69, v57, v58, s0
	v_perm_b32 v57, v57, v58, s1
	v_pk_fma_f16 v58, v67, s36, v60 op_sel_hi:[1,0,1]
	v_pk_fma_f16 v60, v68, s36, v62 op_sel_hi:[1,0,1]
	v_pk_fma_f16 v62, v69, s36, v64 op_sel_hi:[1,0,1]
	v_readlane_b32 s59, v120, 52
	v_lshrrev_b32_e32 v64, 4, v54
	v_pk_fma_f16 v57, v57, s36, v59 op_sel_hi:[1,0,1]
	v_and_b32_e32 v61, 0x7070707, v54
	v_and_b32_e32 v64, 0x7070707, v64
	v_perm_b32 v61, s2, v205, v61
	v_perm_b32 v64, s2, v205, v64
	v_lshlrev_b32_e32 v67, 4, v54
	v_and_or_b32 v61, v67, s4, v61
	v_and_or_b32 v54, v54, s4, v64
	v_perm_b32 v64, v54, v61, s5
	v_perm_b32 v67, v54, v61, s33
	v_perm_b32 v68, v54, v61, s0
	v_perm_b32 v54, v54, v61, s1
	v_pk_fma_f16 v61, v64, s59, v63 op_sel_hi:[1,0,1]
	v_pk_fma_f16 v63, v67, s59, v65 op_sel_hi:[1,0,1]
	v_lshrrev_b32_e32 v65, 4, v55
	v_pk_fma_f16 v54, v54, s59, v56 op_sel_hi:[1,0,1]
	v_and_b32_e32 v56, 0x7070707, v55
	v_and_b32_e32 v65, 0x7070707, v65
	v_pk_fma_f16 v64, v68, s59, v66 op_sel_hi:[1,0,1]
	v_perm_b32 v56, s2, v205, v56
	v_perm_b32 v65, s2, v205, v65
	v_lshlrev_b32_e32 v66, 4, v55
	v_and_or_b32 v56, v66, s4, v56
	v_and_or_b32 v55, v55, s4, v65
	v_perm_b32 v65, v55, v56, s5
	v_perm_b32 v66, v55, v56, s33
	v_perm_b32 v67, v55, v56, s0
	v_perm_b32 v55, v55, v56, s1
	v_pk_fma_f16 v56, v65, s59, v58 op_sel_hi:[1,0,1]
	v_pk_fma_f16 v58, v66, s59, v60 op_sel_hi:[1,0,1]
	v_pk_fma_f16 v60, v67, s59, v62 op_sel_hi:[1,0,1]
	v_readlane_b32 s60, v120, 56
	v_lshrrev_b32_e32 v62, 4, v52
	v_pk_fma_f16 v55, v55, s59, v57 op_sel_hi:[1,0,1]
	v_and_b32_e32 v59, 0x7070707, v52
	v_and_b32_e32 v62, 0x7070707, v62
	v_perm_b32 v59, s2, v205, v59
	v_perm_b32 v62, s2, v205, v62
	v_lshlrev_b32_e32 v65, 4, v52
	v_and_or_b32 v59, v65, s4, v59
	v_and_or_b32 v52, v52, s4, v62
	v_perm_b32 v62, v52, v59, s5
	v_perm_b32 v65, v52, v59, s33
	v_perm_b32 v66, v52, v59, s0
	v_perm_b32 v52, v52, v59, s1
	v_pk_fma_f16 v59, v62, s60, v61 op_sel_hi:[1,0,1]
	v_pk_fma_f16 v61, v65, s60, v63 op_sel_hi:[1,0,1]
	v_lshrrev_b32_e32 v63, 4, v53
	v_pk_fma_f16 v52, v52, s60, v54 op_sel_hi:[1,0,1]
	v_and_b32_e32 v54, 0x7070707, v53
	v_and_b32_e32 v63, 0x7070707, v63
	v_pk_fma_f16 v62, v66, s60, v64 op_sel_hi:[1,0,1]
	v_perm_b32 v54, s2, v205, v54
	v_perm_b32 v63, s2, v205, v63
	v_lshlrev_b32_e32 v64, 4, v53
	v_and_or_b32 v54, v64, s4, v54
	v_and_or_b32 v53, v53, s4, v63
	v_perm_b32 v63, v53, v54, s5
	v_perm_b32 v64, v53, v54, s33
	v_perm_b32 v65, v53, v54, s0
	v_perm_b32 v53, v53, v54, s1
	v_pk_fma_f16 v54, v63, s60, v56 op_sel_hi:[1,0,1]
	v_pk_fma_f16 v56, v64, s60, v58 op_sel_hi:[1,0,1]
	v_pk_fma_f16 v58, v65, s60, v60 op_sel_hi:[1,0,1]
	v_readlane_b32 s36, v120, 60
	v_lshrrev_b32_e32 v60, 4, v36
	v_pk_fma_f16 v53, v53, s60, v55 op_sel_hi:[1,0,1]
	v_and_b32_e32 v57, 0x7070707, v36
	v_and_b32_e32 v60, 0x7070707, v60
	v_perm_b32 v57, s2, v205, v57
	v_perm_b32 v60, s2, v205, v60
	v_lshlrev_b32_e32 v63, 4, v36
	v_and_or_b32 v57, v63, s4, v57
	v_and_or_b32 v36, v36, s4, v60
	v_perm_b32 v60, v36, v57, s5
	v_perm_b32 v63, v36, v57, s33
	v_perm_b32 v64, v36, v57, s0
	v_perm_b32 v36, v36, v57, s1
	v_pk_fma_f16 v100, v36, s36, v52 op_sel_hi:[1,0,1]
	v_lshrrev_b32_e32 v52, 4, v37
	v_and_b32_e32 v36, 0x7070707, v37
	v_and_b32_e32 v52, 0x7070707, v52
	v_perm_b32 v36, s2, v205, v36
	v_perm_b32 v52, s2, v205, v52
	v_lshlrev_b32_e32 v57, 4, v37
	v_and_or_b32 v36, v57, s4, v36
	v_and_or_b32 v37, v37, s4, v52
	v_pk_fma_f16 v103, v60, s36, v59 op_sel_hi:[1,0,1]
	v_perm_b32 v52, v37, v36, s5
	v_perm_b32 v57, v37, v36, s33
	v_perm_b32 v59, v37, v36, s0
	v_perm_b32 v36, v37, v36, s1
	v_pk_fma_f16 v96, v36, s36, v53 op_sel_hi:[1,0,1]
	s_add_u32 s66, s12, s64
	s_addc_u32 s67, s13, s65
	global_load_dwordx2 v[82:83], v121, s[66:67]
	s_add_u32 s66, s14, s64
	s_addc_u32 s67, s15, s65
	global_load_dwordx2 v[80:81], v121, s[66:67]
	s_add_u32 s66, s38, s62
	s_addc_u32 s67, s39, s63
	global_load_dwordx2 v[48:49], v121, s[66:67]
	s_add_u32 s66, s16, s64
	s_addc_u32 s67, s17, s65
	global_load_dwordx2 v[78:79], v121, s[66:67]
	s_add_u32 s66, s50, s62
	s_addc_u32 s67, s51, s63
	global_load_dwordx2 v[46:47], v121, s[66:67]
	s_add_u32 s66, s18, s64
	s_addc_u32 s67, s19, s65
	global_load_dwordx2 v[76:77], v121, s[66:67]
	s_add_u32 s66, s52, s62
	s_addc_u32 s67, s53, s63
	global_load_dwordx2 v[44:45], v121, s[66:67]
	s_add_u32 s66, s20, s64
	s_addc_u32 s67, s21, s65
	global_load_dwordx2 v[74:75], v121, s[66:67]
	s_add_u32 s66, s54, s62
	s_addc_u32 s67, s55, s63
	global_load_dwordx2 v[42:43], v121, s[66:67]
	s_add_u32 s66, s22, s64
	s_addc_u32 s67, s23, s65
	global_load_dwordx2 v[70:71], v121, s[66:67]
	s_add_u32 s66, s56, s62
	s_addc_u32 s67, s57, s63
	global_load_dwordx2 v[40:41], v121, s[66:67]
	v_pk_fma_f16 v101, v64, s36, v62 op_sel_hi:[1,0,1]
	s_add_u32 s66, s24, s64
	s_addc_u32 s67, s25, s65
	global_load_dwordx2 v[68:69], v121, s[66:67]
	s_add_u32 s66, s26, s64
	s_addc_u32 s67, s27, s65
	global_load_dwordx2 v[64:65], v121, s[66:67]
	v_pk_fma_f16 v102, v63, s36, v61 op_sel_hi:[1,0,1]
	s_add_u32 s66, s28, s64
	s_addc_u32 s67, s29, s65
	global_load_dwordx2 v[62:63], v121, s[66:67]
	s_add_u32 s66, s30, s64
	s_addc_u32 s67, s31, s65
	global_load_dwordx2 v[66:67], v121, s[66:67]
	s_add_u32 s66, s34, s64
	s_addc_u32 s67, s35, s65
	global_load_dwordx2 v[60:61], v121, s[66:67]
	v_pk_fma_f16 v97, v59, s36, v58 op_sel_hi:[1,0,1]
	s_add_u32 s66, s38, s64
	s_addc_u32 s67, s39, s65
	global_load_dwordx2 v[58:59], v121, s[66:67]
	v_pk_fma_f16 v98, v57, s36, v56 op_sel_hi:[1,0,1]
	s_add_u32 s66, s50, s64
	s_addc_u32 s67, s51, s65
	global_load_dwordx2 v[56:57], v121, s[66:67]
	v_pk_fma_f16 v99, v52, s36, v54 op_sel_hi:[1,0,1]
	s_add_u32 s66, s52, s64
	s_addc_u32 s67, s53, s65
	global_load_dwordx2 v[54:55], v121, s[66:67]
	s_add_u32 s66, s54, s64
	s_addc_u32 s67, s55, s65
	global_load_dwordx2 v[52:53], v121, s[66:67]
	s_add_u32 s66, s12, s62
	s_addc_u32 s67, s13, s63
	global_load_dwordx2 v[8:9], v121, s[66:67]
	s_add_u32 s66, s14, s62
	s_addc_u32 s67, s15, s63
	global_load_dwordx2 v[10:11], v121, s[66:67]
	s_nop 0
	s_add_u32 s66, s16, s62
	s_addc_u32 s67, s17, s63
	global_load_dwordx2 v[12:13], v121, s[66:67]
	s_nop 0
	s_add_u32 s66, s18, s62
	s_addc_u32 s67, s19, s63
	global_load_dwordx2 v[14:15], v121, s[66:67]
	s_nop 0
	s_add_u32 s66, s20, s62
	s_addc_u32 s67, s21, s63
	global_load_dwordx2 v[16:17], v121, s[66:67]
	s_nop 0
	s_add_u32 s66, s22, s62
	s_addc_u32 s67, s23, s63
	global_load_dwordx2 v[18:19], v121, s[66:67]
	s_nop 0
	s_add_u32 s66, s24, s62
	s_addc_u32 s67, s25, s63
	global_load_dwordx2 v[20:21], v121, s[66:67]
	s_nop 0
	s_add_u32 s66, s26, s62
	s_addc_u32 s67, s27, s63
	global_load_dwordx2 v[22:23], v121, s[66:67]
	s_nop 0
	s_add_u32 s66, s56, s64
	s_addc_u32 s67, s57, s65
	global_load_dwordx2 v[36:37], v121, s[66:67]
	s_cmpk_eq_i32 s58, 0x90
	s_cbranch_scc0 .LBB0_763
	v_lshlrev_b64 v[0:1], 2, v[2:3]
	v_lshl_add_u64 v[2:3], v[28:29], 0, v[0:1]
	v_mov_b32_e32 v104, v208
	v_mov_b32_e32 v105, v209
	v_mov_b32_e32 v106, v210
	v_mov_b32_e32 v107, v211
	v_mov_b32_e32 v108, v212
	v_mov_b32_e32 v109, v213
	v_mov_b32_e32 v110, v214
	v_mov_b32_e32 v111, v215
	v_mov_b32_e32 v86, v216
	v_mov_b32_e32 v87, v217
	v_mov_b32_e32 v88, v218
	v_mov_b32_e32 v89, v219
	v_mov_b32_e32 v112, v220
	v_mov_b32_e32 v113, v221
	v_mov_b32_e32 v114, v222
	v_mov_b32_e32 v115, v223
	v_lshl_add_u64 v[72:73], v[32:33], 0, v[0:1]
	v_cvt_f32_f16_sdwa v1, v103 dst_sel:DWORD dst_unused:UNUSED_PAD src0_sel:WORD_1
	v_cvt_f32_f16_e32 v0, v103
	v_cvt_f32_f16_sdwa v91, v102 dst_sel:DWORD dst_unused:UNUSED_PAD src0_sel:WORD_1
	v_cvt_f32_f16_e32 v90, v102
	v_cvt_f32_f16_sdwa v103, v101 dst_sel:DWORD dst_unused:UNUSED_PAD src0_sel:WORD_1
	v_cvt_f32_f16_e32 v102, v101
	v_cvt_f32_f16_sdwa v101, v100 dst_sel:DWORD dst_unused:UNUSED_PAD src0_sel:WORD_1
	v_cvt_f32_f16_e32 v100, v100
	s_mov_b32 s18, 0x800000
	v_readlane_b32 s12, v255, 5
	v_readlane_b32 s13, v255, 6
	v_pk_add_f32 v[86:87], v[86:87], v[102:103]
	v_pk_add_f32 v[84:85], v[112:113], v[0:1]
	v_mov_b32_e32 v102, v85
	v_mov_b32_e32 v103, v87
	v_pk_add_f32 v[90:91], v[114:115], v[90:91]
	v_pk_add_f32 v[88:89], v[88:89], v[100:101]
	v_mov_b32_e32 v100, v84
	v_mov_b32_e32 v101, v86
	v_pk_mul_f32 v[102:103], v[102:103], v[102:103]
	v_mov_b32_e32 v112, v91
	v_pk_fma_f32 v[100:101], v[100:101], v[100:101], v[102:103]
	v_mov_b32_e32 v102, v90
	v_mov_b32_e32 v103, v88
	v_pk_fma_f32 v[100:101], v[102:103], v[102:103], v[100:101]
	v_cvt_f32_f16_sdwa v103, v99 dst_sel:DWORD dst_unused:UNUSED_PAD src0_sel:WORD_1
	v_cvt_f32_f16_e32 v102, v99
	v_cvt_f32_f16_sdwa v99, v98 dst_sel:DWORD dst_unused:UNUSED_PAD src0_sel:WORD_1
	v_cvt_f32_f16_e32 v98, v98
	v_mov_b32_e32 v113, v89
	v_pk_add_f32 v[102:103], v[108:109], v[102:103]
	v_cvt_f32_f16_sdwa v109, v97 dst_sel:DWORD dst_unused:UNUSED_PAD src0_sel:WORD_1
	v_cvt_f32_f16_e32 v108, v97
	v_cvt_f32_f16_sdwa v97, v96 dst_sel:DWORD dst_unused:UNUSED_PAD src0_sel:WORD_1
	v_cvt_f32_f16_e32 v96, v96
	v_pk_add_f32 v[98:99], v[110:111], v[98:99]
	v_pk_add_f32 v[104:105], v[104:105], v[108:109]
	v_mov_b32_e32 v108, v103
	v_mov_b32_e32 v109, v105
	v_pk_add_f32 v[96:97], v[106:107], v[96:97]
	v_mov_b32_e32 v106, v102
	v_mov_b32_e32 v107, v104
	v_pk_mul_f32 v[108:109], v[108:109], v[108:109]
	v_pk_fma_f32 v[100:101], v[112:113], v[112:113], v[100:101]
	v_pk_fma_f32 v[106:107], v[106:107], v[106:107], v[108:109]
	v_mov_b32_e32 v108, v98
	v_mov_b32_e32 v109, v96
	v_mov_b32_e32 v110, v99
	v_mov_b32_e32 v111, v97
	v_pk_fma_f32 v[106:107], v[108:109], v[108:109], v[106:107]
	v_add_f32_e32 v95, v100, v101
	v_pk_fma_f32 v[106:107], v[110:111], v[110:111], v[106:107]
	v_lshl_add_u64 v[34:35], v[34:35], 0, s[12:13]
	v_add_f32_e32 v95, v95, v106
	v_add_f32_e32 v95, v95, v107
	v_mov_b32_e32 v100, v95
	s_nop 1
	v_permlane32_swap_b32 v100, v95
	s_waitcnt lgkmcnt(0)
	v_add_f32_e32 v95, v95, v100
	v_mov_b32_e32 v100, v95
	s_nop 1
	v_permlane16_swap_b32 v100, v95
	s_waitcnt lgkmcnt(0)
	v_add_f32_e32 v95, v95, v100
	s_nop 1
	v_mov_b32_dpp v100, v95 row_ror:8 row_mask:0xf bank_mask:0xf
	s_waitcnt lgkmcnt(0)
	v_add_f32_e32 v95, v95, v100
	s_nop 1
	v_mov_b32_dpp v100, v95 row_half_mirror row_mask:0xf bank_mask:0xf
	s_nop 1
	v_mov_b32_dpp v100, v100 quad_perm:[3,2,1,0] row_mask:0xf bank_mask:0xf
	s_waitcnt lgkmcnt(0)
	v_add_f32_e32 v95, v95, v100
	s_nop 1
	v_mov_b32_dpp v100, v95 quad_perm:[2,3,0,1] row_mask:0xf bank_mask:0xf
	s_waitcnt lgkmcnt(0)
	v_add_f32_e32 v95, v95, v100
	s_nop 1
	v_mov_b32_dpp v100, v95 quad_perm:[1,0,3,2] row_mask:0xf bank_mask:0xf
	s_waitcnt lgkmcnt(0)
	v_add_f32_e32 v95, v95, v100
	v_fmamk_f32 v95, v95, 0x3a800000, v191
	v_cmp_gt_f32_e32 vcc, s18, v95
	v_mul_f32_e32 v100, 0x4b800000, v95
	s_nop 0
	v_cndmask_b32_e32 v95, v95, v100, vcc
	v_rsq_f32_e32 v95, v95
	s_nop 0
	v_mul_f32_e32 v100, 0x45800000, v95
	v_cndmask_b32_e32 v100, v95, v100, vcc
	v_pk_mul_f32 v[84:85], v[84:85], v[100:101] op_sel_hi:[1,0]
	v_pk_mul_f32 v[0:1], v[124:125], v[84:85]
	v_pk_mul_f32 v[84:85], v[90:91], v[100:101] op_sel_hi:[1,0]
	s_nop 0
	v_pk_mul_f32 v[2:3], v[126:127], v[84:85]
	global_store_dwordx4 v[72:73], v[0:3], off
	s_nop 1
	v_pk_mul_f32 v[84:85], v[86:87], v[100:101] op_sel_hi:[1,0]
	v_pk_mul_f32 v[0:1], v[128:129], v[84:85]
	v_pk_mul_f32 v[84:85], v[88:89], v[100:101] op_sel_hi:[1,0]
	s_nop 0
	v_pk_mul_f32 v[2:3], v[130:131], v[84:85]
	global_store_dwordx4 v[72:73], v[0:3], off offset:16
	s_nop 1
	v_pk_mul_f32 v[84:85], v[102:103], v[100:101] op_sel_hi:[1,0]
	v_pk_mul_f32 v[0:1], v[84:85], v[132:133]
	v_pk_mul_f32 v[84:85], v[98:99], v[100:101] op_sel_hi:[1,0]
	s_nop 0
	v_pk_mul_f32 v[2:3], v[84:85], v[134:135]
	global_store_dwordx4 v[72:73], v[0:3], off offset:32
	s_nop 1
	v_pk_mul_f32 v[84:85], v[104:105], v[100:101] op_sel_hi:[1,0]
	v_pk_mul_f32 v[0:1], v[84:85], v[136:137]
	v_pk_mul_f32 v[84:85], v[96:97], v[100:101] op_sel_hi:[1,0]
	s_nop 0
	v_pk_mul_f32 v[2:3], v[84:85], v[138:139]
	global_store_dwordx4 v[72:73], v[0:3], off offset:48
	s_nop 1
	v_mov_b32_e32 v0, v94
	s_andn2_b64 exec, exec, s[10:11]
	s_cbranch_execnz .LBB0_762

.LBB0_767:
	v_readlane_b32 s8, v253, 0
	v_readlane_b32 s9, v253, 1
	v_mov_b32_e32 v3, v175
	v_readlane_b32 s6, v253, 8
	v_ashrrev_i32_e32 v0, 6, v3
	s_nop 0
	v_add_u32_e32 v0, s6, v0
	v_cmp_gt_i32_e32 vcc, s87, v0
	s_and_saveexec_b64 s[6:7], vcc
	s_mov_b32 s12, 0x800000
	s_cbranch_execz .LBB0_772
	v_ashrrev_i32_e32 v1, 31, v0
	v_and_b32_e32 v2, 15, v3
	v_lshlrev_b64 v[4:5], 9, v[0:1]
	v_lshl_add_u64 v[8:9], s[94:95], 0, v[4:5]
	v_lshlrev_b32_e32 v144, 2, v2
	v_lshl_add_u64 v[8:9], v[8:9], 0, v[144:145]
	global_load_dword v96, v[8:9], off
	v_and_b32_e32 v6, 63, v3
	v_readlane_b32 s10, v253, 27
	v_lshlrev_b32_e32 v144, 3, v6
	v_readlane_b32 s11, v253, 28
	s_load_dwordx2 s[8:9], s[8:9], 0x10
	v_and_b32_e32 v1, 32, v3
	v_lshl_add_u64 v[16:17], s[10:11], 0, v[144:145]
	v_readlane_b32 s10, v253, 29
	v_readlane_b32 s11, v253, 30
	v_cmp_eq_u32_e64 s[40:41], 0, v1
	v_and_b32_e32 v1, 16, v3
	v_lshl_add_u64 v[18:19], s[10:11], 0, v[144:145]
	v_lshlrev_b32_e32 v144, 5, v6
	v_and_b32_e32 v97, 60, v3
	v_cmp_eq_u32_e64 s[42:43], 0, v1
	v_and_b32_e32 v1, 8, v3
	v_cmp_eq_u32_e64 s[44:45], 0, v1
	v_and_b32_e32 v1, 4, v3
	v_or_b32_e32 v4, v4, v97
	v_cmp_eq_u32_e64 s[46:47], 0, v1
	s_waitcnt vmcnt(0)
	v_readlane_b32 s10, v96, 0
	s_ashr_i32 s11, s10, 31
	s_lshl_b64 s[10:11], s[10:11], 9
	v_lshl_add_u64 v[8:9], v[16:17], 0, s[10:11]
	global_load_dwordx2 v[20:21], v[8:9], off
	v_lshl_add_u64 v[8:9], v[18:19], 0, s[10:11]
	v_readlane_b32 s10, v96, 1
	s_ashr_i32 s11, s10, 31
	s_lshl_b64 s[10:11], s[10:11], 9
	global_load_dwordx2 v[92:93], v[8:9], off
	v_lshl_add_u64 v[8:9], v[16:17], 0, s[10:11]
	global_load_dwordx2 v[22:23], v[8:9], off
	v_lshl_add_u64 v[8:9], v[18:19], 0, s[10:11]
	v_readlane_b32 s10, v96, 2
	s_ashr_i32 s11, s10, 31
	s_lshl_b64 s[10:11], s[10:11], 9
	global_load_dwordx2 v[90:91], v[8:9], off
	v_lshl_add_u64 v[8:9], v[16:17], 0, s[10:11]
	global_load_dwordx2 v[24:25], v[8:9], off
	v_lshl_add_u64 v[8:9], v[18:19], 0, s[10:11]
	v_readlane_b32 s10, v96, 3
	s_ashr_i32 s11, s10, 31
	s_lshl_b64 s[10:11], s[10:11], 9
	global_load_dwordx2 v[88:89], v[8:9], off
	v_lshl_add_u64 v[8:9], v[16:17], 0, s[10:11]
	global_load_dwordx2 v[26:27], v[8:9], off
	v_lshl_add_u64 v[8:9], v[18:19], 0, s[10:11]
	v_readlane_b32 s10, v96, 4
	s_ashr_i32 s11, s10, 31
	s_lshl_b64 s[10:11], s[10:11], 9
	global_load_dwordx2 v[86:87], v[8:9], off
	v_lshl_add_u64 v[8:9], v[16:17], 0, s[10:11]
	global_load_dwordx2 v[28:29], v[8:9], off
	v_lshl_add_u64 v[8:9], v[18:19], 0, s[10:11]
	v_readlane_b32 s10, v96, 5
	s_ashr_i32 s11, s10, 31
	s_lshl_b64 s[10:11], s[10:11], 9
	global_load_dwordx2 v[84:85], v[8:9], off
	v_lshl_add_u64 v[8:9], v[16:17], 0, s[10:11]
	global_load_dwordx2 v[30:31], v[8:9], off
	v_lshl_add_u64 v[8:9], v[18:19], 0, s[10:11]
	v_readlane_b32 s10, v96, 6
	s_ashr_i32 s11, s10, 31
	s_lshl_b64 s[10:11], s[10:11], 9
	global_load_dwordx2 v[82:83], v[8:9], off
	v_lshl_add_u64 v[8:9], v[16:17], 0, s[10:11]
	global_load_dwordx2 v[32:33], v[8:9], off
	v_lshl_add_u64 v[8:9], v[18:19], 0, s[10:11]
	v_readlane_b32 s10, v96, 7
	s_ashr_i32 s11, s10, 31
	s_lshl_b64 s[10:11], s[10:11], 9
	global_load_dwordx2 v[80:81], v[8:9], off
	v_lshl_add_u64 v[8:9], v[16:17], 0, s[10:11]
	global_load_dwordx2 v[34:35], v[8:9], off
	v_lshl_add_u64 v[8:9], v[18:19], 0, s[10:11]
	v_readlane_b32 s10, v96, 8
	s_ashr_i32 s11, s10, 31
	s_lshl_b64 s[10:11], s[10:11], 9
	global_load_dwordx2 v[78:79], v[8:9], off
	v_lshl_add_u64 v[8:9], v[16:17], 0, s[10:11]
	global_load_dwordx2 v[36:37], v[8:9], off
	v_lshl_add_u64 v[8:9], v[18:19], 0, s[10:11]
	v_readlane_b32 s10, v96, 9
	s_ashr_i32 s11, s10, 31
	s_lshl_b64 s[10:11], s[10:11], 9
	global_load_dwordx2 v[76:77], v[8:9], off
	v_lshl_add_u64 v[8:9], v[16:17], 0, s[10:11]
	global_load_dwordx2 v[38:39], v[8:9], off
	v_lshl_add_u64 v[8:9], v[18:19], 0, s[10:11]
	v_readlane_b32 s10, v96, 10
	s_ashr_i32 s11, s10, 31
	s_lshl_b64 s[10:11], s[10:11], 9
	global_load_dwordx2 v[70:71], v[8:9], off
	v_lshl_add_u64 v[8:9], v[16:17], 0, s[10:11]
	global_load_dwordx2 v[40:41], v[8:9], off
	v_lshl_add_u64 v[8:9], v[18:19], 0, s[10:11]
	v_readlane_b32 s10, v96, 11
	s_ashr_i32 s11, s10, 31
	s_lshl_b64 s[10:11], s[10:11], 9
	global_load_dwordx2 v[66:67], v[8:9], off
	v_lshl_add_u64 v[8:9], v[16:17], 0, s[10:11]
	global_load_dwordx2 v[60:61], v[8:9], off
	v_lshl_add_u64 v[8:9], v[18:19], 0, s[10:11]
	v_readlane_b32 s10, v96, 12
	s_ashr_i32 s11, s10, 31
	s_lshl_b64 s[10:11], s[10:11], 9
	global_load_dwordx2 v[72:73], v[8:9], off
	v_lshl_add_u64 v[8:9], v[16:17], 0, s[10:11]
	global_load_dwordx2 v[58:59], v[8:9], off
	v_lshl_add_u64 v[8:9], v[18:19], 0, s[10:11]
	v_readlane_b32 s10, v96, 13
	s_ashr_i32 s11, s10, 31
	s_lshl_b64 s[10:11], s[10:11], 9
	global_load_dwordx2 v[68:69], v[8:9], off
	v_lshl_add_u64 v[8:9], v[16:17], 0, s[10:11]
	global_load_dwordx2 v[56:57], v[8:9], off
	v_lshl_add_u64 v[8:9], v[18:19], 0, s[10:11]
	v_readlane_b32 s10, v96, 14
	s_ashr_i32 s11, s10, 31
	s_lshl_b64 s[10:11], s[10:11], 9
	global_load_dwordx2 v[64:65], v[8:9], off
	v_lshl_add_u64 v[8:9], v[16:17], 0, s[10:11]
	global_load_dwordx2 v[54:55], v[8:9], off
	v_lshl_add_u64 v[8:9], v[18:19], 0, s[10:11]
	v_readlane_b32 s10, v96, 15
	s_ashr_i32 s11, s10, 31
	s_lshl_b64 s[10:11], s[10:11], 9
	global_load_dwordx2 v[62:63], v[8:9], off
	v_lshl_add_u64 v[8:9], v[16:17], 0, s[10:11]
	global_load_dwordx2 v[52:53], v[8:9], off
	v_lshl_add_u64 v[8:9], v[18:19], 0, s[10:11]
	global_load_dwordx2 v[50:51], v[8:9], off
	v_readlane_b32 s10, v253, 15
	v_readlane_b32 s11, v253, 16
	s_nop 1
	v_lshl_add_u64 v[42:43], s[10:11], 0, v[144:145]
	v_lshlrev_b32_e32 v144, 6, v6
	s_waitcnt lgkmcnt(0)
	v_lshl_add_u64 v[6:7], s[8:9], 0, v[144:145]
	s_mov_b64 s[8:9], 0x1000
	v_readlane_b32 s10, v253, 13
	v_lshl_add_u64 v[46:47], v[6:7], 0, s[8:9]
	v_readlane_b32 s8, v253, 23
	v_readlane_b32 s11, v253, 14
	v_readlane_b32 s9, v253, 24
	s_nop 0
	v_lshl_add_u64 v[44:45], s[10:11], 0, v[144:145]
	v_lshl_add_u64 v[48:49], s[8:9], 0, v[4:5]
	s_mov_b64 s[8:9], 0
	v_lshlrev_b32_e32 v144, 2, v2
	v_readfirstlane_b32 s62, v16
	v_readfirstlane_b32 s63, v17
	v_readfirstlane_b32 s64, v18
	v_readfirstlane_b32 s65, v19
	v_and_b32_e32 v121, 63, v175
	v_lshlrev_b32_e32 v121, 3, v121

.LBB0_770:
	s_cmpk_eq_i32 s56, 0x80
	s_cselect_b64 s[10:11], -1, 0
	ds_bpermute_b32 v6, v97, v96
	s_and_b64 vcc, s[10:11], s[48:49]
	v_cndmask_b32_e32 v94, v0, v98, vcc
	v_ashrrev_i32_e32 v95, 31, v94
	s_and_b32 s10, s56, 0x70
	v_lshlrev_b64 v[94:95], 9, v[94:95]
	v_lshl_add_u64 v[94:95], s[94:95], 0, v[94:95]
	s_lshl_b32 s36, s10, 2
	s_waitcnt lgkmcnt(0)
	v_ashrrev_i32_e32 v7, 31, v6
	v_lshl_add_u64 v[94:95], v[94:95], 0, s[36:37]
	v_lshl_add_u64 v[6:7], v[6:7], 3, s[88:89]
	v_lshl_add_u64 v[94:95], v[94:95], 0, v[144:145]
	global_load_dwordx2 v[6:7], v[6:7], off
	s_nop 0
	global_load_dword v8, v[4:5], off
	global_load_dword v96, v[94:95], off
	s_waitcnt vmcnt(33)
	v_dot8_i32_i4 v9, v20, v1, 0
	v_dot8_i32_i4 v94, v20, v10, 0
	v_dot8_i32_i4 v9, v21, v11, v9
	v_dot8_i32_i4 v94, v21, v12, v94
	v_dot8_i32_i4 v20, v22, v1, 0
	v_dot8_i32_i4 v21, v22, v10, 0
	v_dot8_i32_i4 v20, v23, v11, v20
	v_dot8_i32_i4 v21, v23, v12, v21
	v_lshl_add_u32 v9, v9, 4, v94
	v_cvt_f32_i32_e32 v9, v9
	s_add_i32 s56, s56, 16
	v_lshl_add_u32 v20, v20, 4, v21
	v_cvt_f32_i32_e32 v94, v20
	s_waitcnt vmcnt(32)
	v_dot8_i32_i4 v20, v24, v1, 0
	v_dot8_i32_i4 v21, v24, v10, 0
	v_dot8_i32_i4 v20, v25, v11, v20
	v_dot8_i32_i4 v21, v25, v12, v21
	v_lshl_add_u64 v[4:5], v[4:5], 0, 64
	s_waitcnt vmcnt(2)
	v_mul_f32_e32 v7, v13, v7
	v_lshl_add_u32 v20, v20, 4, v21
	v_cvt_f32_i32_e32 v95, v20
	v_dot8_i32_i4 v20, v26, v1, 0
	v_dot8_i32_i4 v21, v26, v10, 0
	v_dot8_i32_i4 v20, v27, v11, v20
	v_dot8_i32_i4 v21, v27, v12, v21
	s_waitcnt vmcnt(0)
	v_readlane_b32 s10, v96, 0
	s_ashr_i32 s11, s10, 31
	v_readlane_b32 s12, v96, 1
	v_lshl_add_u32 v20, v20, 4, v21
	v_cvt_f32_i32_e32 v106, v20
	v_dot8_i32_i4 v20, v28, v1, 0
	v_dot8_i32_i4 v21, v28, v10, 0
	v_dot8_i32_i4 v20, v29, v11, v20
	v_dot8_i32_i4 v21, v29, v12, v21
	s_lshl_b64 s[10:11], s[10:11], 9
	s_ashr_i32 s13, s12, 31
	v_readlane_b32 s14, v96, 2
	v_lshl_add_u32 v20, v20, 4, v21
	v_cvt_f32_i32_e32 v107, v20
	v_dot8_i32_i4 v20, v30, v1, 0
	v_dot8_i32_i4 v21, v30, v10, 0
	v_dot8_i32_i4 v20, v31, v11, v20
	v_dot8_i32_i4 v21, v31, v12, v21
	s_lshl_b64 s[12:13], s[12:13], 9
	s_ashr_i32 s15, s14, 31
	v_readlane_b32 s16, v96, 3
	v_lshl_add_u32 v20, v20, 4, v21
	v_cvt_f32_i32_e32 v108, v20
	v_dot8_i32_i4 v20, v32, v1, 0
	v_dot8_i32_i4 v21, v32, v10, 0
	v_dot8_i32_i4 v20, v33, v11, v20
	v_dot8_i32_i4 v21, v33, v12, v21
	s_lshl_b64 s[14:15], s[14:15], 9
	s_ashr_i32 s17, s16, 31
	s_nop 0
	v_lshl_add_u32 v20, v20, 4, v21
	v_cvt_f32_i32_e32 v109, v20
	v_dot8_i32_i4 v20, v34, v1, 0
	v_dot8_i32_i4 v21, v34, v10, 0
	v_dot8_i32_i4 v20, v35, v11, v20
	v_dot8_i32_i4 v21, v35, v12, v21
	v_readlane_b32 s18, v96, 4
	s_add_u32 s66, s12, s62
	s_addc_u32 s67, s13, s63
	global_load_dwordx2 v[22:23], v121, s[66:67]
	v_lshl_add_u32 v20, v20, 4, v21
	v_cvt_f32_i32_e32 v110, v20
	v_dot8_i32_i4 v20, v36, v1, 0
	v_dot8_i32_i4 v21, v36, v10, 0
	v_dot8_i32_i4 v20, v37, v11, v20
	v_dot8_i32_i4 v21, v37, v12, v21
	s_lshl_b64 s[16:17], s[16:17], 9
	s_ashr_i32 s19, s18, 31
	v_readlane_b32 s20, v96, 5
	v_lshl_add_u32 v20, v20, 4, v21
	v_cvt_f32_i32_e32 v111, v20
	v_dot8_i32_i4 v20, v38, v1, 0
	v_dot8_i32_i4 v21, v38, v10, 0
	v_dot8_i32_i4 v20, v39, v11, v20
	v_dot8_i32_i4 v21, v39, v12, v21
	v_permlane32_swap_b32 v9, v111
	s_nop 1
	v_lshl_add_u32 v20, v20, 4, v21
	v_cvt_f32_i32_e32 v112, v20
	v_dot8_i32_i4 v20, v40, v1, 0
	v_dot8_i32_i4 v21, v40, v10, 0
	v_dot8_i32_i4 v20, v41, v11, v20
	v_dot8_i32_i4 v21, v41, v12, v21
	s_waitcnt lgkmcnt(0)
	v_add_f32_e32 v9, v9, v111
	v_permlane32_swap_b32 v94, v112
	v_lshl_add_u32 v20, v20, 4, v21
	v_cvt_f32_i32_e32 v113, v20
	v_dot8_i32_i4 v20, v60, v1, 0
	v_dot8_i32_i4 v21, v60, v10, 0
	v_dot8_i32_i4 v20, v61, v11, v20
	v_dot8_i32_i4 v21, v61, v12, v21
	s_waitcnt lgkmcnt(0)
	v_add_f32_e32 v94, v94, v112
	v_permlane32_swap_b32 v95, v113
	v_lshl_add_u32 v20, v20, 4, v21
	v_cvt_f32_i32_e32 v114, v20
	v_dot8_i32_i4 v20, v58, v1, 0
	v_dot8_i32_i4 v21, v58, v10, 0
	v_dot8_i32_i4 v20, v59, v11, v20
	v_dot8_i32_i4 v21, v59, v12, v21
	s_waitcnt lgkmcnt(0)
	v_add_f32_e32 v95, v95, v113
	v_permlane32_swap_b32 v106, v114
	v_lshl_add_u32 v20, v20, 4, v21
	v_cvt_f32_i32_e32 v115, v20
	v_dot8_i32_i4 v20, v56, v1, 0
	v_dot8_i32_i4 v21, v56, v10, 0
	v_dot8_i32_i4 v20, v57, v11, v20
	v_dot8_i32_i4 v21, v57, v12, v21
	s_waitcnt lgkmcnt(0)
	v_add_f32_e32 v106, v106, v114
	v_permlane32_swap_b32 v107, v115
	v_lshl_add_u32 v20, v20, 4, v21
	v_cvt_f32_i32_e32 v116, v20
	v_dot8_i32_i4 v20, v54, v1, 0
	v_dot8_i32_i4 v21, v54, v10, 0
	v_dot8_i32_i4 v20, v55, v11, v20
	v_dot8_i32_i4 v21, v55, v12, v21
	s_waitcnt lgkmcnt(0)
	v_add_f32_e32 v107, v107, v115
	v_permlane32_swap_b32 v108, v116
	v_lshl_add_u32 v20, v20, 4, v21
	v_cvt_f32_i32_e32 v117, v20
	v_dot8_i32_i4 v20, v52, v1, 0
	v_dot8_i32_i4 v21, v52, v10, 0
	v_dot8_i32_i4 v20, v53, v11, v20
	v_dot8_i32_i4 v21, v53, v12, v21
	s_waitcnt lgkmcnt(0)
	v_add_f32_e32 v108, v108, v116
	v_permlane32_swap_b32 v109, v117
	v_lshl_add_u32 v20, v20, 4, v21
	v_cvt_f32_i32_e32 v118, v20
	s_waitcnt lgkmcnt(0)
	v_add_f32_e32 v109, v109, v117
	v_permlane32_swap_b32 v110, v118
	s_add_u32 s66, s10, s62
	s_addc_u32 s67, s11, s63
	global_load_dwordx2 v[20:21], v121, s[66:67]
	s_add_u32 s66, s14, s62
	s_addc_u32 s67, s15, s63
	global_load_dwordx2 v[24:25], v121, s[66:67]
	s_waitcnt lgkmcnt(0)
	v_add_f32_e32 v110, v110, v118
	v_permlane16_swap_b32 v9, v107
	s_lshl_b64 s[18:19], s[18:19], 9
	s_ashr_i32 s21, s20, 31
	v_readlane_b32 s22, v96, 6
	s_add_u32 s66, s16, s62
	s_addc_u32 s67, s17, s63
	global_load_dwordx2 v[26:27], v121, s[66:67]
	s_waitcnt lgkmcnt(0)
	v_add_f32_e32 v9, v9, v107
	v_permlane16_swap_b32 v94, v108
	s_lshl_b64 s[20:21], s[20:21], 9
	s_ashr_i32 s23, s22, 31
	s_waitcnt lgkmcnt(0)
	v_add_f32_e32 v94, v94, v108
	v_permlane16_swap_b32 v95, v109
	v_readlane_b32 s24, v96, 7
	s_add_u32 s66, s18, s62
	s_addc_u32 s67, s19, s63
	global_load_dwordx2 v[28:29], v121, s[66:67]
	s_waitcnt lgkmcnt(0)
	v_add_f32_e32 v95, v95, v109
	v_permlane16_swap_b32 v106, v110
	s_lshl_b64 s[22:23], s[22:23], 9
	s_ashr_i32 s25, s24, 31
	v_readlane_b32 s26, v96, 8
	s_waitcnt lgkmcnt(0)
	v_add_f32_e32 v106, v106, v110
	v_cndmask_b32_e64 v107, v9, v95, s[44:45]
	v_cndmask_b32_e64 v9, v95, v9, s[44:45]
	s_nop 0
	v_mov_b32_dpp v95, v107 row_ror:8 row_mask:0xf bank_mask:0xf
	s_add_u32 s66, s20, s62
	s_addc_u32 s67, s21, s63
	global_load_dwordx2 v[30:31], v121, s[66:67]
	s_lshl_b64 s[24:25], s[24:25], 9
	s_ashr_i32 s27, s26, 31
	s_waitcnt lgkmcnt(0)
	v_add_f32_e32 v9, v9, v95
	v_cndmask_b32_e64 v95, v94, v106, s[44:45]
	s_nop 1
	v_mov_b32_dpp v95, v95 row_ror:8 row_mask:0xf bank_mask:0xf
	v_cndmask_b32_e64 v94, v106, v94, s[44:45]
	v_readlane_b32 s28, v96, 9
	s_add_u32 s66, s22, s62
	s_addc_u32 s67, s23, s63
	global_load_dwordx2 v[32:33], v121, s[66:67]
	s_waitcnt lgkmcnt(0)
	v_add_f32_e32 v94, v94, v95
	v_cndmask_b32_e64 v95, v9, v94, s[46:47]
	v_cndmask_b32_e64 v9, v94, v9, s[46:47]
	s_nop 0
	v_mov_b32_dpp v94, v95 row_half_mirror row_mask:0xf bank_mask:0xf
	s_nop 1
	v_mov_b32_dpp v94, v94 quad_perm:[3,2,1,0] row_mask:0xf bank_mask:0xf
	s_lshl_b64 s[26:27], s[26:27], 9
	s_ashr_i32 s29, s28, 31
	v_readlane_b32 s30, v96, 10
	s_add_u32 s66, s24, s62
	s_addc_u32 s67, s25, s63
	global_load_dwordx2 v[34:35], v121, s[66:67]
	s_waitcnt lgkmcnt(0)
	v_add_f32_e32 v9, v9, v94
	s_nop 1
	v_mov_b32_dpp v94, v9 quad_perm:[2,3,0,1] row_mask:0xf bank_mask:0xf
	s_lshl_b64 s[28:29], s[28:29], 9
	s_ashr_i32 s31, s30, 31
	v_readlane_b32 s34, v96, 11
	s_waitcnt lgkmcnt(0)
	v_add_f32_e32 v9, v9, v94
	s_nop 1
	v_mov_b32_dpp v94, v9 quad_perm:[1,0,3,2] row_mask:0xf bank_mask:0xf
	s_add_u32 s66, s26, s62
	s_addc_u32 s67, s27, s63
	global_load_dwordx2 v[36:37], v121, s[66:67]
	s_lshl_b64 s[30:31], s[30:31], 9
	s_ashr_i32 s35, s34, 31
	s_waitcnt lgkmcnt(0)
	v_add_f32_e32 v9, v9, v94
	v_add_f32_e32 v9, v14, v9
	v_mul_f32_e32 v7, v7, v9
	v_mul_f32_e32 v9, 0x3d372713, v7
	v_mul_f32_e32 v9, v7, v9
	v_fma_f32 v9, v7, v9, v7
	v_mul_f32_e32 v9, 0x3fcc422a, v9
	v_mul_f32_e32 v9, 0xbfb8aa3b, v9
	v_exp_f32_e32 v9, v9
	v_lshlrev_b32_e32 v94, 4, v92
	v_readlane_b32 s38, v96, 12
	s_add_u32 s66, s28, s62
	s_addc_u32 s67, s29, s63
	global_load_dwordx2 v[38:39], v121, s[66:67]
	v_add_f32_e32 v9, 1.0, v9
	v_rcp_f32_e32 v9, v9
	s_lshl_b64 s[34:35], s[34:35], 9
	s_ashr_i32 s39, s38, 31
	v_pk_mul_f32 v[6:7], v[6:7], v[8:9]
	v_lshrrev_b32_e32 v9, 4, v92
	v_pk_mul_f32 v[6:7], v[6:7], v[6:7] op_sel:[0,1] op_sel_hi:[1,0]
	v_cvt_f16_f32_e32 v120, v6
	v_and_b32_e32 v8, 0x7070707, v92
	v_readlane_b32 s36, v120, 0
	v_and_b32_e32 v9, 0x7070707, v9
	v_perm_b32 v8, s2, v205, v8
	v_perm_b32 v9, s2, v205, v9
	v_and_or_b32 v8, v94, s4, v8
	v_and_or_b32 v9, v92, s4, v9
	v_perm_b32 v92, v9, v8, s5
	v_perm_b32 v94, v9, v8, s33
	v_perm_b32 v95, v9, v8, s0
	v_perm_b32 v8, v9, v8, s1
	v_pk_fma_f16 v8, v8, s36, v102 op_sel_hi:[1,0,1]
	v_lshrrev_b32_e32 v102, 4, v93
	v_pk_fma_f16 v9, v92, s36, v105 op_sel_hi:[1,0,1]
	v_pk_fma_f16 v92, v94, s36, v104 op_sel_hi:[1,0,1]
	v_pk_fma_f16 v94, v95, s36, v103 op_sel_hi:[1,0,1]
	v_and_b32_e32 v95, 0x7070707, v93
	v_and_b32_e32 v102, 0x7070707, v102
	v_perm_b32 v95, s2, v205, v95
	v_perm_b32 v102, s2, v205, v102
	v_lshlrev_b32_e32 v103, 4, v93
	v_and_or_b32 v95, v103, s4, v95
	v_and_or_b32 v93, v93, s4, v102
	v_perm_b32 v102, v93, v95, s5
	v_perm_b32 v103, v93, v95, s33
	v_perm_b32 v104, v93, v95, s0
	v_perm_b32 v93, v93, v95, s1
	v_pk_fma_f16 v95, v102, s36, v101 op_sel_hi:[1,0,1]
	v_readlane_b32 s59, v120, 4
	v_lshrrev_b32_e32 v101, 4, v90
	v_pk_fma_f16 v100, v103, s36, v100 op_sel_hi:[1,0,1]
	v_pk_fma_f16 v99, v104, s36, v99 op_sel_hi:[1,0,1]
	v_pk_fma_f16 v7, v93, s36, v15 op_sel_hi:[1,0,1]
	v_and_b32_e32 v93, 0x7070707, v90
	v_and_b32_e32 v101, 0x7070707, v101
	v_perm_b32 v93, s2, v205, v93
	v_perm_b32 v101, s2, v205, v101
	v_lshlrev_b32_e32 v102, 4, v90
	v_and_or_b32 v93, v102, s4, v93
	v_and_or_b32 v90, v90, s4, v101
	v_perm_b32 v103, v90, v93, s0
	v_perm_b32 v101, v90, v93, s5
	v_perm_b32 v102, v90, v93, s33
	v_perm_b32 v90, v90, v93, s1
	v_pk_fma_f16 v93, v103, s59, v94 op_sel_hi:[1,0,1]
	v_lshrrev_b32_e32 v94, 4, v91
	v_pk_fma_f16 v8, v90, s59, v8 op_sel_hi:[1,0,1]
	v_and_b32_e32 v90, 0x7070707, v91
	v_and_b32_e32 v94, 0x7070707, v94
	v_pk_fma_f16 v9, v101, s59, v9 op_sel_hi:[1,0,1]
	v_perm_b32 v90, s2, v205, v90
	v_perm_b32 v94, s2, v205, v94
	v_lshlrev_b32_e32 v101, 4, v91
	v_and_or_b32 v90, v101, s4, v90
	v_and_or_b32 v91, v91, s4, v94
	v_pk_fma_f16 v92, v102, s59, v92 op_sel_hi:[1,0,1]
	v_perm_b32 v94, v91, v90, s5
	v_perm_b32 v102, v91, v90, s0
	v_perm_b32 v101, v91, v90, s33
	v_perm_b32 v90, v91, v90, s1
	v_pk_fma_f16 v91, v94, s59, v95 op_sel_hi:[1,0,1]
	v_pk_fma_f16 v95, v102, s59, v99 op_sel_hi:[1,0,1]
	v_readlane_b32 s60, v120, 8
	v_lshrrev_b32_e32 v99, 4, v88
	v_pk_fma_f16 v94, v101, s59, v100 op_sel_hi:[1,0,1]
	v_pk_fma_f16 v7, v90, s59, v7 op_sel_hi:[1,0,1]
	v_and_b32_e32 v90, 0x7070707, v88
	v_and_b32_e32 v99, 0x7070707, v99
	v_perm_b32 v90, s2, v205, v90
	v_perm_b32 v99, s2, v205, v99
	v_lshlrev_b32_e32 v100, 4, v88
	v_and_or_b32 v90, v100, s4, v90
	v_and_or_b32 v88, v88, s4, v99
	v_perm_b32 v100, v88, v90, s33
	v_perm_b32 v101, v88, v90, s0
	v_perm_b32 v99, v88, v90, s5
	v_perm_b32 v88, v88, v90, s1
	v_pk_fma_f16 v90, v100, s60, v92 op_sel_hi:[1,0,1]
	v_pk_fma_f16 v92, v101, s60, v93 op_sel_hi:[1,0,1]
	v_lshrrev_b32_e32 v93, 4, v89
	v_pk_fma_f16 v8, v88, s60, v8 op_sel_hi:[1,0,1]
	v_and_b32_e32 v88, 0x7070707, v89
	v_and_b32_e32 v93, 0x7070707, v93
	v_pk_fma_f16 v9, v99, s60, v9 op_sel_hi:[1,0,1]
	v_perm_b32 v88, s2, v205, v88
	v_perm_b32 v93, s2, v205, v93
	v_lshlrev_b32_e32 v99, 4, v89
	v_and_or_b32 v88, v99, s4, v88
	v_and_or_b32 v89, v89, s4, v93
	v_perm_b32 v93, v89, v88, s5
	v_perm_b32 v99, v89, v88, s33
	v_perm_b32 v100, v89, v88, s0
	v_perm_b32 v88, v89, v88, s1
	v_pk_fma_f16 v89, v93, s60, v91 op_sel_hi:[1,0,1]
	v_pk_fma_f16 v91, v99, s60, v94 op_sel_hi:[1,0,1]
	v_readlane_b32 s36, v120, 12
	v_lshrrev_b32_e32 v94, 4, v86
	v_pk_fma_f16 v93, v100, s60, v95 op_sel_hi:[1,0,1]
	v_pk_fma_f16 v7, v88, s60, v7 op_sel_hi:[1,0,1]
	v_and_b32_e32 v88, 0x7070707, v86
	v_and_b32_e32 v94, 0x7070707, v94
	v_perm_b32 v88, s2, v205, v88
	v_perm_b32 v94, s2, v205, v94
	v_lshlrev_b32_e32 v95, 4, v86
	v_and_or_b32 v88, v95, s4, v88
	v_and_or_b32 v86, v86, s4, v94
	v_perm_b32 v95, v86, v88, s33
	v_perm_b32 v99, v86, v88, s0
	v_perm_b32 v94, v86, v88, s5
	v_perm_b32 v86, v86, v88, s1
	v_pk_fma_f16 v88, v95, s36, v90 op_sel_hi:[1,0,1]
	v_pk_fma_f16 v90, v99, s36, v92 op_sel_hi:[1,0,1]
	v_lshrrev_b32_e32 v92, 4, v87
	v_pk_fma_f16 v8, v86, s36, v8 op_sel_hi:[1,0,1]
	v_and_b32_e32 v86, 0x7070707, v87
	v_and_b32_e32 v92, 0x7070707, v92
	v_pk_fma_f16 v9, v94, s36, v9 op_sel_hi:[1,0,1]
	v_perm_b32 v86, s2, v205, v86
	v_perm_b32 v92, s2, v205, v92
	v_lshlrev_b32_e32 v94, 4, v87
	v_and_or_b32 v86, v94, s4, v86
	v_and_or_b32 v87, v87, s4, v92
	v_perm_b32 v92, v87, v86, s5
	v_perm_b32 v94, v87, v86, s33
	v_perm_b32 v95, v87, v86, s0
	v_perm_b32 v86, v87, v86, s1
	v_pk_fma_f16 v87, v92, s36, v89 op_sel_hi:[1,0,1]
	v_readlane_b32 s59, v120, 16
	v_lshrrev_b32_e32 v92, 4, v84
	v_pk_fma_f16 v89, v94, s36, v91 op_sel_hi:[1,0,1]
	v_pk_fma_f16 v91, v95, s36, v93 op_sel_hi:[1,0,1]
	v_pk_fma_f16 v7, v86, s36, v7 op_sel_hi:[1,0,1]
	v_and_b32_e32 v86, 0x7070707, v84
	v_and_b32_e32 v92, 0x7070707, v92
	v_perm_b32 v86, s2, v205, v86
	v_perm_b32 v92, s2, v205, v92
	v_lshlrev_b32_e32 v93, 4, v84
	v_and_or_b32 v86, v93, s4, v86
	v_and_or_b32 v84, v84, s4, v92
	v_perm_b32 v93, v84, v86, s33
	v_perm_b32 v94, v84, v86, s0
	v_perm_b32 v92, v84, v86, s5
	v_perm_b32 v84, v84, v86, s1
	v_pk_fma_f16 v86, v93, s59, v88 op_sel_hi:[1,0,1]
	v_pk_fma_f16 v88, v94, s59, v90 op_sel_hi:[1,0,1]
	v_lshrrev_b32_e32 v90, 4, v85
	v_pk_fma_f16 v8, v84, s59, v8 op_sel_hi:[1,0,1]
	v_and_b32_e32 v84, 0x7070707, v85
	v_and_b32_e32 v90, 0x7070707, v90
	v_pk_fma_f16 v9, v92, s59, v9 op_sel_hi:[1,0,1]
	v_perm_b32 v84, s2, v205, v84
	v_perm_b32 v90, s2, v205, v90
	v_lshlrev_b32_e32 v92, 4, v85
	v_and_or_b32 v84, v92, s4, v84
	v_and_or_b32 v85, v85, s4, v90
	v_perm_b32 v90, v85, v84, s5
	v_perm_b32 v92, v85, v84, s33
	v_perm_b32 v93, v85, v84, s0
	v_perm_b32 v84, v85, v84, s1
	v_pk_fma_f16 v85, v90, s59, v87 op_sel_hi:[1,0,1]
	v_readlane_b32 s60, v120, 20
	v_lshrrev_b32_e32 v90, 4, v82
	v_pk_fma_f16 v87, v92, s59, v89 op_sel_hi:[1,0,1]
	v_pk_fma_f16 v89, v93, s59, v91 op_sel_hi:[1,0,1]
	v_pk_fma_f16 v7, v84, s59, v7 op_sel_hi:[1,0,1]
	v_and_b32_e32 v84, 0x7070707, v82
	v_and_b32_e32 v90, 0x7070707, v90
	v_perm_b32 v84, s2, v205, v84
	v_perm_b32 v90, s2, v205, v90
	v_lshlrev_b32_e32 v91, 4, v82
	v_and_or_b32 v84, v91, s4, v84
	v_and_or_b32 v82, v82, s4, v90
	v_perm_b32 v91, v82, v84, s33
	v_perm_b32 v92, v82, v84, s0
	v_perm_b32 v90, v82, v84, s5
	v_perm_b32 v82, v82, v84, s1
	v_pk_fma_f16 v84, v91, s60, v86 op_sel_hi:[1,0,1]
	v_pk_fma_f16 v86, v92, s60, v88 op_sel_hi:[1,0,1]
	v_lshrrev_b32_e32 v88, 4, v83
	v_pk_fma_f16 v8, v82, s60, v8 op_sel_hi:[1,0,1]
	v_and_b32_e32 v82, 0x7070707, v83
	v_and_b32_e32 v88, 0x7070707, v88
	v_pk_fma_f16 v9, v90, s60, v9 op_sel_hi:[1,0,1]
	v_perm_b32 v82, s2, v205, v82
	v_perm_b32 v88, s2, v205, v88
	v_lshlrev_b32_e32 v90, 4, v83
	v_and_or_b32 v82, v90, s4, v82
	v_and_or_b32 v83, v83, s4, v88
	v_perm_b32 v88, v83, v82, s5
	v_perm_b32 v90, v83, v82, s33
	v_perm_b32 v91, v83, v82, s0
	v_perm_b32 v82, v83, v82, s1
	v_pk_fma_f16 v83, v88, s60, v85 op_sel_hi:[1,0,1]
	v_readlane_b32 s36, v120, 24
	v_lshrrev_b32_e32 v88, 4, v80
	v_pk_fma_f16 v85, v90, s60, v87 op_sel_hi:[1,0,1]
	v_pk_fma_f16 v87, v91, s60, v89 op_sel_hi:[1,0,1]
	v_pk_fma_f16 v7, v82, s60, v7 op_sel_hi:[1,0,1]
	v_and_b32_e32 v82, 0x7070707, v80
	v_and_b32_e32 v88, 0x7070707, v88
	v_perm_b32 v82, s2, v205, v82
	v_perm_b32 v88, s2, v205, v88
	v_lshlrev_b32_e32 v89, 4, v80
	v_and_or_b32 v82, v89, s4, v82
	v_and_or_b32 v80, v80, s4, v88
	v_perm_b32 v89, v80, v82, s33
	v_perm_b32 v90, v80, v82, s0
	v_perm_b32 v88, v80, v82, s5
	v_perm_b32 v80, v80, v82, s1
	v_pk_fma_f16 v82, v89, s36, v84 op_sel_hi:[1,0,1]
	v_pk_fma_f16 v84, v90, s36, v86 op_sel_hi:[1,0,1]
	v_lshrrev_b32_e32 v86, 4, v81
	v_pk_fma_f16 v8, v80, s36, v8 op_sel_hi:[1,0,1]
	v_and_b32_e32 v80, 0x7070707, v81
	v_and_b32_e32 v86, 0x7070707, v86
	v_pk_fma_f16 v9, v88, s36, v9 op_sel_hi:[1,0,1]
	v_perm_b32 v80, s2, v205, v80
	v_perm_b32 v86, s2, v205, v86
	v_lshlrev_b32_e32 v88, 4, v81
	v_and_or_b32 v80, v88, s4, v80
	v_and_or_b32 v81, v81, s4, v86
	v_perm_b32 v86, v81, v80, s5
	v_perm_b32 v88, v81, v80, s33
	v_perm_b32 v89, v81, v80, s0
	v_perm_b32 v80, v81, v80, s1
	v_pk_fma_f16 v81, v86, s36, v83 op_sel_hi:[1,0,1]
	v_readlane_b32 s59, v120, 28
	v_lshrrev_b32_e32 v86, 4, v78
	v_pk_fma_f16 v83, v88, s36, v85 op_sel_hi:[1,0,1]
	v_pk_fma_f16 v85, v89, s36, v87 op_sel_hi:[1,0,1]
	v_pk_fma_f16 v7, v80, s36, v7 op_sel_hi:[1,0,1]
	v_and_b32_e32 v80, 0x7070707, v78
	v_and_b32_e32 v86, 0x7070707, v86
	v_perm_b32 v80, s2, v205, v80
	v_perm_b32 v86, s2, v205, v86
	v_lshlrev_b32_e32 v87, 4, v78
	v_and_or_b32 v80, v87, s4, v80
	v_and_or_b32 v78, v78, s4, v86
	v_perm_b32 v87, v78, v80, s33
	v_perm_b32 v88, v78, v80, s0
	v_perm_b32 v86, v78, v80, s5
	v_perm_b32 v78, v78, v80, s1
	v_pk_fma_f16 v80, v87, s59, v82 op_sel_hi:[1,0,1]
	v_pk_fma_f16 v82, v88, s59, v84 op_sel_hi:[1,0,1]
	v_lshrrev_b32_e32 v84, 4, v79
	v_pk_fma_f16 v8, v78, s59, v8 op_sel_hi:[1,0,1]
	v_and_b32_e32 v78, 0x7070707, v79
	v_and_b32_e32 v84, 0x7070707, v84
	v_pk_fma_f16 v9, v86, s59, v9 op_sel_hi:[1,0,1]
	v_perm_b32 v78, s2, v205, v78
	v_perm_b32 v84, s2, v205, v84
	v_lshlrev_b32_e32 v86, 4, v79
	v_and_or_b32 v78, v86, s4, v78
	v_and_or_b32 v79, v79, s4, v84
	v_perm_b32 v84, v79, v78, s5
	v_perm_b32 v86, v79, v78, s33
	v_perm_b32 v87, v79, v78, s0
	v_perm_b32 v78, v79, v78, s1
	v_pk_fma_f16 v79, v84, s59, v81 op_sel_hi:[1,0,1]
	v_readlane_b32 s60, v120, 32
	v_lshrrev_b32_e32 v84, 4, v76
	v_pk_fma_f16 v81, v86, s59, v83 op_sel_hi:[1,0,1]
	v_pk_fma_f16 v83, v87, s59, v85 op_sel_hi:[1,0,1]
	v_pk_fma_f16 v7, v78, s59, v7 op_sel_hi:[1,0,1]
	v_and_b32_e32 v78, 0x7070707, v76
	v_and_b32_e32 v84, 0x7070707, v84
	v_perm_b32 v78, s2, v205, v78
	v_perm_b32 v84, s2, v205, v84
	v_lshlrev_b32_e32 v85, 4, v76
	v_and_or_b32 v78, v85, s4, v78
	v_and_or_b32 v76, v76, s4, v84
	v_perm_b32 v85, v76, v78, s33
	v_perm_b32 v86, v76, v78, s0
	v_perm_b32 v84, v76, v78, s5
	v_perm_b32 v76, v76, v78, s1
	v_pk_fma_f16 v78, v85, s60, v80 op_sel_hi:[1,0,1]
	v_pk_fma_f16 v80, v86, s60, v82 op_sel_hi:[1,0,1]
	v_lshrrev_b32_e32 v82, 4, v77
	v_pk_fma_f16 v8, v76, s60, v8 op_sel_hi:[1,0,1]
	v_and_b32_e32 v76, 0x7070707, v77
	v_and_b32_e32 v82, 0x7070707, v82
	v_pk_fma_f16 v9, v84, s60, v9 op_sel_hi:[1,0,1]
	v_perm_b32 v76, s2, v205, v76
	v_perm_b32 v82, s2, v205, v82
	v_lshlrev_b32_e32 v84, 4, v77
	v_and_or_b32 v76, v84, s4, v76
	v_and_or_b32 v77, v77, s4, v82
	v_perm_b32 v82, v77, v76, s5
	v_perm_b32 v84, v77, v76, s33
	v_perm_b32 v85, v77, v76, s0
	v_perm_b32 v76, v77, v76, s1
	v_pk_fma_f16 v77, v82, s60, v79 op_sel_hi:[1,0,1]
	v_readlane_b32 s36, v120, 36
	v_lshrrev_b32_e32 v82, 4, v70
	v_pk_fma_f16 v79, v84, s60, v81 op_sel_hi:[1,0,1]
	v_pk_fma_f16 v81, v85, s60, v83 op_sel_hi:[1,0,1]
	v_pk_fma_f16 v7, v76, s60, v7 op_sel_hi:[1,0,1]
	v_and_b32_e32 v76, 0x7070707, v70
	v_and_b32_e32 v82, 0x7070707, v82
	v_perm_b32 v76, s2, v205, v76
	v_perm_b32 v82, s2, v205, v82
	v_lshlrev_b32_e32 v83, 4, v70
	v_and_or_b32 v76, v83, s4, v76
	v_and_or_b32 v70, v70, s4, v82
	v_perm_b32 v83, v70, v76, s33
	v_perm_b32 v84, v70, v76, s0
	v_perm_b32 v82, v70, v76, s5
	v_perm_b32 v70, v70, v76, s1
	v_pk_fma_f16 v76, v83, s36, v78 op_sel_hi:[1,0,1]
	v_pk_fma_f16 v78, v84, s36, v80 op_sel_hi:[1,0,1]
	v_lshrrev_b32_e32 v80, 4, v71
	v_pk_fma_f16 v8, v70, s36, v8 op_sel_hi:[1,0,1]
	v_and_b32_e32 v70, 0x7070707, v71
	v_and_b32_e32 v80, 0x7070707, v80
	v_pk_fma_f16 v9, v82, s36, v9 op_sel_hi:[1,0,1]
	v_perm_b32 v70, s2, v205, v70
	v_perm_b32 v80, s2, v205, v80
	v_lshlrev_b32_e32 v82, 4, v71
	v_and_or_b32 v70, v82, s4, v70
	v_and_or_b32 v71, v71, s4, v80
	v_perm_b32 v80, v71, v70, s5
	v_perm_b32 v82, v71, v70, s33
	v_perm_b32 v83, v71, v70, s0
	v_perm_b32 v70, v71, v70, s1
	v_pk_fma_f16 v71, v80, s36, v77 op_sel_hi:[1,0,1]
	v_readlane_b32 s59, v120, 40
	v_lshrrev_b32_e32 v80, 4, v66
	v_pk_fma_f16 v77, v82, s36, v79 op_sel_hi:[1,0,1]
	v_pk_fma_f16 v79, v83, s36, v81 op_sel_hi:[1,0,1]
	v_pk_fma_f16 v7, v70, s36, v7 op_sel_hi:[1,0,1]
	v_and_b32_e32 v70, 0x7070707, v66
	v_and_b32_e32 v80, 0x7070707, v80
	v_perm_b32 v70, s2, v205, v70
	v_perm_b32 v80, s2, v205, v80
	v_lshlrev_b32_e32 v81, 4, v66
	v_and_or_b32 v70, v81, s4, v70
	v_and_or_b32 v66, v66, s4, v80
	v_perm_b32 v81, v66, v70, s33
	v_perm_b32 v82, v66, v70, s0
	v_perm_b32 v80, v66, v70, s5
	v_perm_b32 v66, v66, v70, s1
	v_pk_fma_f16 v70, v81, s59, v76 op_sel_hi:[1,0,1]
	v_pk_fma_f16 v76, v82, s59, v78 op_sel_hi:[1,0,1]
	v_lshrrev_b32_e32 v78, 4, v67
	v_pk_fma_f16 v8, v66, s59, v8 op_sel_hi:[1,0,1]
	v_and_b32_e32 v66, 0x7070707, v67
	v_and_b32_e32 v78, 0x7070707, v78
	v_pk_fma_f16 v9, v80, s59, v9 op_sel_hi:[1,0,1]
	v_perm_b32 v66, s2, v205, v66
	v_perm_b32 v78, s2, v205, v78
	v_lshlrev_b32_e32 v80, 4, v67
	v_and_or_b32 v66, v80, s4, v66
	v_and_or_b32 v67, v67, s4, v78
	v_perm_b32 v78, v67, v66, s5
	v_perm_b32 v80, v67, v66, s33
	v_perm_b32 v81, v67, v66, s0
	v_perm_b32 v66, v67, v66, s1
	v_pk_fma_f16 v67, v78, s59, v71 op_sel_hi:[1,0,1]
	v_readlane_b32 s60, v120, 44
	v_lshrrev_b32_e32 v78, 4, v72
	v_pk_fma_f16 v71, v80, s59, v77 op_sel_hi:[1,0,1]
	v_pk_fma_f16 v77, v81, s59, v79 op_sel_hi:[1,0,1]
	v_pk_fma_f16 v7, v66, s59, v7 op_sel_hi:[1,0,1]
	v_and_b32_e32 v66, 0x7070707, v72
	v_and_b32_e32 v78, 0x7070707, v78
	v_perm_b32 v66, s2, v205, v66
	v_perm_b32 v78, s2, v205, v78
	v_lshlrev_b32_e32 v79, 4, v72
	v_and_or_b32 v66, v79, s4, v66
	v_and_or_b32 v72, v72, s4, v78
	v_perm_b32 v80, v72, v66, s0
	v_perm_b32 v78, v72, v66, s5
	v_perm_b32 v79, v72, v66, s33
	v_perm_b32 v66, v72, v66, s1
	v_pk_fma_f16 v72, v80, s60, v76 op_sel_hi:[1,0,1]
	v_lshrrev_b32_e32 v76, 4, v73
	v_pk_fma_f16 v8, v66, s60, v8 op_sel_hi:[1,0,1]
	v_and_b32_e32 v66, 0x7070707, v73
	v_and_b32_e32 v76, 0x7070707, v76
	v_pk_fma_f16 v9, v78, s60, v9 op_sel_hi:[1,0,1]
	v_perm_b32 v66, s2, v205, v66
	v_perm_b32 v76, s2, v205, v76
	v_lshlrev_b32_e32 v78, 4, v73
	v_and_or_b32 v66, v78, s4, v66
	v_and_or_b32 v73, v73, s4, v76
	v_perm_b32 v76, v73, v66, s5
	v_pk_fma_f16 v70, v79, s60, v70 op_sel_hi:[1,0,1]
	v_perm_b32 v78, v73, v66, s33
	v_perm_b32 v79, v73, v66, s0
	v_perm_b32 v66, v73, v66, s1
	v_pk_fma_f16 v67, v76, s60, v67 op_sel_hi:[1,0,1]
	v_readlane_b32 s36, v120, 48
	v_lshrrev_b32_e32 v76, 4, v68
	v_pk_fma_f16 v71, v78, s60, v71 op_sel_hi:[1,0,1]
	v_pk_fma_f16 v73, v79, s60, v77 op_sel_hi:[1,0,1]
	v_pk_fma_f16 v7, v66, s60, v7 op_sel_hi:[1,0,1]
	v_and_b32_e32 v66, 0x7070707, v68
	v_and_b32_e32 v76, 0x7070707, v76
	v_perm_b32 v66, s2, v205, v66
	v_perm_b32 v76, s2, v205, v76
	v_lshlrev_b32_e32 v77, 4, v68
	v_and_or_b32 v66, v77, s4, v66
	v_and_or_b32 v68, v68, s4, v76
	v_perm_b32 v77, v68, v66, s33
	v_perm_b32 v78, v68, v66, s0
	v_perm_b32 v76, v68, v66, s5
	v_perm_b32 v66, v68, v66, s1
	v_pk_fma_f16 v68, v77, s36, v70 op_sel_hi:[1,0,1]
	v_pk_fma_f16 v70, v78, s36, v72 op_sel_hi:[1,0,1]
	v_lshrrev_b32_e32 v72, 4, v69
	v_pk_fma_f16 v8, v66, s36, v8 op_sel_hi:[1,0,1]
	v_and_b32_e32 v66, 0x7070707, v69
	v_and_b32_e32 v72, 0x7070707, v72
	v_pk_fma_f16 v9, v76, s36, v9 op_sel_hi:[1,0,1]
	v_perm_b32 v66, s2, v205, v66
	v_perm_b32 v72, s2, v205, v72
	v_lshlrev_b32_e32 v76, 4, v69
	v_and_or_b32 v66, v76, s4, v66
	v_and_or_b32 v69, v69, s4, v72
	v_perm_b32 v72, v69, v66, s5
	v_perm_b32 v76, v69, v66, s33
	v_perm_b32 v77, v69, v66, s0
	v_perm_b32 v66, v69, v66, s1
	v_pk_fma_f16 v67, v72, s36, v67 op_sel_hi:[1,0,1]
	v_readlane_b32 s59, v120, 52
	v_lshrrev_b32_e32 v72, 4, v64
	v_pk_fma_f16 v69, v76, s36, v71 op_sel_hi:[1,0,1]
	v_pk_fma_f16 v71, v77, s36, v73 op_sel_hi:[1,0,1]
	v_pk_fma_f16 v7, v66, s36, v7 op_sel_hi:[1,0,1]
	v_and_b32_e32 v66, 0x7070707, v64
	v_and_b32_e32 v72, 0x7070707, v72
	v_perm_b32 v66, s2, v205, v66
	v_perm_b32 v72, s2, v205, v72
	v_lshlrev_b32_e32 v73, 4, v64
	v_and_or_b32 v66, v73, s4, v66
	v_and_or_b32 v64, v64, s4, v72
	v_perm_b32 v73, v64, v66, s33
	v_perm_b32 v76, v64, v66, s0
	v_perm_b32 v72, v64, v66, s5
	v_perm_b32 v64, v64, v66, s1
	v_pk_fma_f16 v66, v73, s59, v68 op_sel_hi:[1,0,1]
	v_pk_fma_f16 v68, v76, s59, v70 op_sel_hi:[1,0,1]
	v_lshrrev_b32_e32 v70, 4, v65
	v_pk_fma_f16 v8, v64, s59, v8 op_sel_hi:[1,0,1]
	v_and_b32_e32 v64, 0x7070707, v65
	v_and_b32_e32 v70, 0x7070707, v70
	v_pk_fma_f16 v9, v72, s59, v9 op_sel_hi:[1,0,1]
	v_perm_b32 v64, s2, v205, v64
	v_perm_b32 v70, s2, v205, v70
	v_lshlrev_b32_e32 v72, 4, v65
	v_and_or_b32 v64, v72, s4, v64
	v_and_or_b32 v65, v65, s4, v70
	v_perm_b32 v70, v65, v64, s5
	v_perm_b32 v72, v65, v64, s33
	v_perm_b32 v73, v65, v64, s0
	v_perm_b32 v64, v65, v64, s1
	v_pk_fma_f16 v65, v70, s59, v67 op_sel_hi:[1,0,1]
	v_readlane_b32 s60, v120, 56
	v_lshrrev_b32_e32 v70, 4, v62
	v_pk_fma_f16 v67, v72, s59, v69 op_sel_hi:[1,0,1]
	v_pk_fma_f16 v69, v73, s59, v71 op_sel_hi:[1,0,1]
	v_pk_fma_f16 v7, v64, s59, v7 op_sel_hi:[1,0,1]
	v_and_b32_e32 v64, 0x7070707, v62
	v_and_b32_e32 v70, 0x7070707, v70
	v_perm_b32 v64, s2, v205, v64
	v_perm_b32 v70, s2, v205, v70
	v_lshlrev_b32_e32 v71, 4, v62
	v_and_or_b32 v64, v71, s4, v64
	v_and_or_b32 v62, v62, s4, v70
	v_perm_b32 v71, v62, v64, s33
	v_perm_b32 v72, v62, v64, s0
	v_perm_b32 v70, v62, v64, s5
	v_perm_b32 v62, v62, v64, s1
	v_pk_fma_f16 v64, v71, s60, v66 op_sel_hi:[1,0,1]
	v_pk_fma_f16 v66, v72, s60, v68 op_sel_hi:[1,0,1]
	v_lshrrev_b32_e32 v68, 4, v63
	v_pk_fma_f16 v8, v62, s60, v8 op_sel_hi:[1,0,1]
	v_and_b32_e32 v62, 0x7070707, v63
	v_and_b32_e32 v68, 0x7070707, v68
	v_pk_fma_f16 v9, v70, s60, v9 op_sel_hi:[1,0,1]
	v_perm_b32 v62, s2, v205, v62
	v_perm_b32 v68, s2, v205, v68
	v_lshlrev_b32_e32 v70, 4, v63
	v_and_or_b32 v62, v70, s4, v62
	v_and_or_b32 v63, v63, s4, v68
	v_perm_b32 v68, v63, v62, s5
	v_perm_b32 v70, v63, v62, s33
	v_perm_b32 v71, v63, v62, s0
	v_perm_b32 v62, v63, v62, s1
	v_pk_fma_f16 v7, v62, s60, v7 op_sel_hi:[1,0,1]
	v_readlane_b32 s36, v120, 60
	v_lshrrev_b32_e32 v62, 4, v50
	v_pk_fma_f16 v63, v68, s60, v65 op_sel_hi:[1,0,1]
	v_pk_fma_f16 v65, v70, s60, v67 op_sel_hi:[1,0,1]
	v_pk_fma_f16 v67, v71, s60, v69 op_sel_hi:[1,0,1]
	v_and_b32_e32 v15, 0x7070707, v50
	v_and_b32_e32 v62, 0x7070707, v62
	v_perm_b32 v15, s2, v205, v15
	v_perm_b32 v62, s2, v205, v62
	v_lshlrev_b32_e32 v68, 4, v50
	v_and_or_b32 v15, v68, s4, v15
	v_and_or_b32 v50, v50, s4, v62
	v_perm_b32 v62, v50, v15, s5
	v_perm_b32 v68, v50, v15, s33
	v_perm_b32 v69, v50, v15, s0
	v_perm_b32 v15, v50, v15, s1
	v_pk_fma_f16 v105, v62, s36, v9 op_sel_hi:[1,0,1]
	v_lshrrev_b32_e32 v9, 4, v51
	v_pk_fma_f16 v102, v15, s36, v8 op_sel_hi:[1,0,1]
	v_and_b32_e32 v8, 0x7070707, v51
	v_and_b32_e32 v9, 0x7070707, v9
	v_perm_b32 v8, s2, v205, v8
	v_perm_b32 v9, s2, v205, v9
	v_lshlrev_b32_e32 v15, 4, v51
	v_and_or_b32 v8, v15, s4, v8
	v_and_or_b32 v9, v51, s4, v9
	v_perm_b32 v15, v9, v8, s5
	v_perm_b32 v50, v9, v8, s33
	v_perm_b32 v51, v9, v8, s0
	v_perm_b32 v8, v9, v8, s1
	v_pk_fma_f16 v104, v68, s36, v64 op_sel_hi:[1,0,1]
	v_pk_fma_f16 v103, v69, s36, v66 op_sel_hi:[1,0,1]
	v_pk_fma_f16 v101, v15, s36, v63 op_sel_hi:[1,0,1]
	v_pk_fma_f16 v100, v50, s36, v65 op_sel_hi:[1,0,1]
	v_pk_fma_f16 v99, v51, s36, v67 op_sel_hi:[1,0,1]
	v_pk_fma_f16 v15, v8, s36, v7 op_sel_hi:[1,0,1]
	s_add_u32 s66, s10, s64
	s_addc_u32 s67, s11, s65
	global_load_dwordx2 v[92:93], v121, s[66:67]
	s_add_u32 s66, s12, s64
	s_addc_u32 s67, s13, s65
	global_load_dwordx2 v[90:91], v121, s[66:67]
	s_add_u32 s66, s14, s64
	s_addc_u32 s67, s15, s65
	global_load_dwordx2 v[88:89], v121, s[66:67]
	s_add_u32 s66, s16, s64
	s_addc_u32 s67, s17, s65
	global_load_dwordx2 v[86:87], v121, s[66:67]
	s_add_u32 s66, s18, s64
	s_addc_u32 s67, s19, s65
	global_load_dwordx2 v[84:85], v121, s[66:67]
	s_add_u32 s66, s20, s64
	s_addc_u32 s67, s21, s65
	global_load_dwordx2 v[82:83], v121, s[66:67]
	s_add_u32 s66, s22, s64
	s_addc_u32 s67, s23, s65
	global_load_dwordx2 v[80:81], v121, s[66:67]
	s_add_u32 s66, s24, s64
	s_addc_u32 s67, s25, s65
	global_load_dwordx2 v[78:79], v121, s[66:67]
	s_add_u32 s66, s26, s64
	s_addc_u32 s67, s27, s65
	global_load_dwordx2 v[76:77], v121, s[66:67]
	v_readlane_b32 s50, v96, 13
	s_add_u32 s66, s28, s64
	s_addc_u32 s67, s29, s65
	global_load_dwordx2 v[70:71], v121, s[66:67]
	s_add_u32 s66, s30, s62
	s_addc_u32 s67, s31, s63
	global_load_dwordx2 v[40:41], v121, s[66:67]
	s_lshl_b64 s[38:39], s[38:39], 9
	s_ashr_i32 s51, s50, 31
	v_readlane_b32 s52, v96, 14
	s_add_u32 s66, s30, s64
	s_addc_u32 s67, s31, s65
	global_load_dwordx2 v[66:67], v121, s[66:67]
	s_add_u32 s66, s34, s62
	s_addc_u32 s67, s35, s63
	global_load_dwordx2 v[60:61], v121, s[66:67]
	s_add_u32 s66, s34, s64
	s_addc_u32 s67, s35, s65
	global_load_dwordx2 v[72:73], v121, s[66:67]
	s_lshl_b64 s[50:51], s[50:51], 9
	s_ashr_i32 s53, s52, 31
	v_readlane_b32 s54, v96, 15
	s_add_u32 s66, s38, s62
	s_addc_u32 s67, s39, s63
	global_load_dwordx2 v[58:59], v121, s[66:67]
	s_add_u32 s66, s38, s64
	s_addc_u32 s67, s39, s65
	global_load_dwordx2 v[68:69], v121, s[66:67]
	s_lshl_b64 s[52:53], s[52:53], 9
	s_ashr_i32 s55, s54, 31
	s_add_u32 s66, s50, s62
	s_addc_u32 s67, s51, s63
	global_load_dwordx2 v[56:57], v121, s[66:67]
	s_add_u32 s66, s50, s64
	s_addc_u32 s67, s51, s65
	global_load_dwordx2 v[64:65], v121, s[66:67]
	s_lshl_b64 s[54:55], s[54:55], 9
	s_add_u32 s66, s52, s62
	s_addc_u32 s67, s53, s63
	global_load_dwordx2 v[54:55], v121, s[66:67]
	s_add_u32 s66, s52, s64
	s_addc_u32 s67, s53, s65
	global_load_dwordx2 v[62:63], v121, s[66:67]
	s_add_u32 s66, s54, s62
	s_addc_u32 s67, s55, s63
	global_load_dwordx2 v[52:53], v121, s[66:67]
	s_add_u32 s66, s54, s64
	s_addc_u32 s67, s55, s65
	global_load_dwordx2 v[50:51], v121, s[66:67]
	s_cmpk_eq_i32 s56, 0x90
	s_cbranch_scc0 .LBB0_770
	v_lshl_add_u64 v[94:95], v[2:3], 2, v[44:45]
	v_mov_b32_e32 v106, v208
	v_mov_b32_e32 v107, v209
	v_mov_b32_e32 v108, v210
	v_mov_b32_e32 v109, v211
	v_mov_b32_e32 v8, v212
	v_mov_b32_e32 v9, v213
	v_mov_b32_e32 v10, v214
	v_mov_b32_e32 v11, v215
	v_mov_b32_e32 v4, v216
	v_mov_b32_e32 v5, v217
	v_mov_b32_e32 v6, v218
	v_mov_b32_e32 v7, v219
	v_mov_b32_e32 v0, v220
	v_mov_b32_e32 v1, v221
	v_mov_b32_e32 v2, v222
	v_mov_b32_e32 v3, v223
	v_cvt_f32_f16_sdwa v13, v105 dst_sel:DWORD dst_unused:UNUSED_PAD src0_sel:WORD_1
	v_cvt_f32_f16_e32 v12, v105
	s_mov_b32 s12, 0x800000
	v_readlane_b32 s10, v255, 5
	v_readlane_b32 s11, v255, 6
	v_pk_add_f32 v[0:1], v[0:1], v[12:13]
	v_cvt_f32_f16_sdwa v13, v104 dst_sel:DWORD dst_unused:UNUSED_PAD src0_sel:WORD_1
	v_cvt_f32_f16_e32 v12, v104
	v_lshl_add_u64 v[48:49], v[48:49], 0, s[10:11]
	v_pk_add_f32 v[2:3], v[2:3], v[12:13]
	v_cvt_f32_f16_sdwa v13, v103 dst_sel:DWORD dst_unused:UNUSED_PAD src0_sel:WORD_1
	v_cvt_f32_f16_e32 v12, v103
	global_store_dwordx4 v[94:95], v[0:3], off
	v_pk_add_f32 v[4:5], v[4:5], v[12:13]
	v_cvt_f32_f16_sdwa v13, v102 dst_sel:DWORD dst_unused:UNUSED_PAD src0_sel:WORD_1
	v_cvt_f32_f16_e32 v12, v102
	v_mov_b32_e32 v102, v1
	v_mov_b32_e32 v103, v5
	v_pk_mul_f32 v[102:103], v[102:103], v[102:103]
	v_pk_add_f32 v[6:7], v[6:7], v[12:13]
	v_mov_b32_e32 v12, v0
	v_mov_b32_e32 v13, v4
	v_pk_fma_f32 v[12:13], v[12:13], v[12:13], v[102:103]
	v_mov_b32_e32 v102, v2
	v_mov_b32_e32 v103, v6
	v_pk_fma_f32 v[12:13], v[102:103], v[102:103], v[12:13]
	v_mov_b32_e32 v102, v3
	v_mov_b32_e32 v103, v7
	v_pk_fma_f32 v[102:103], v[102:103], v[102:103], v[12:13]
	v_cvt_f32_f16_sdwa v13, v101 dst_sel:DWORD dst_unused:UNUSED_PAD src0_sel:WORD_1
	v_cvt_f32_f16_e32 v12, v101
	v_cvt_f32_f16_sdwa v101, v15 dst_sel:DWORD dst_unused:UNUSED_PAD src0_sel:WORD_1
	global_store_dwordx4 v[94:95], v[4:7], off offset:16
	v_pk_add_f32 v[8:9], v[8:9], v[12:13]
	v_cvt_f32_f16_sdwa v13, v100 dst_sel:DWORD dst_unused:UNUSED_PAD src0_sel:WORD_1
	v_cvt_f32_f16_e32 v12, v100
	v_cvt_f32_f16_e32 v100, v15
	v_pk_add_f32 v[10:11], v[10:11], v[12:13]
	v_cvt_f32_f16_sdwa v13, v99 dst_sel:DWORD dst_unused:UNUSED_PAD src0_sel:WORD_1
	v_cvt_f32_f16_e32 v12, v99
	v_pk_add_f32 v[14:15], v[108:109], v[100:101]
	v_mov_b32_e32 v100, v9
	global_store_dwordx4 v[94:95], v[8:11], off offset:32
	v_pk_add_f32 v[12:13], v[106:107], v[12:13]
	global_store_dwordx4 v[94:95], v[12:15], off offset:48
	v_mov_b32_e32 v101, v13
	v_mov_b32_e32 v94, v8
	v_mov_b32_e32 v95, v12
	v_pk_mul_f32 v[100:101], v[100:101], v[100:101]
	v_add_f32_e32 v99, v102, v103
	v_pk_fma_f32 v[94:95], v[94:95], v[94:95], v[100:101]
	v_mov_b32_e32 v100, v10
	v_mov_b32_e32 v101, v14
	v_pk_fma_f32 v[94:95], v[100:101], v[100:101], v[94:95]
	v_mov_b32_e32 v100, v11
	v_mov_b32_e32 v101, v15
	v_pk_fma_f32 v[94:95], v[100:101], v[100:101], v[94:95]
	global_load_dwordx4 v[100:103], v[46:47], off offset:48
	global_load_dwordx4 v[104:107], v[46:47], off offset:32
	global_load_dwordx4 v[108:111], v[46:47], off offset:16
	global_load_dwordx4 v[112:115], v[46:47], off
	v_add_f32_e32 v94, v99, v94
	v_add_f32_e32 v94, v94, v95
	v_mov_b32_e32 v95, v94
	s_nop 1
	v_permlane32_swap_b32 v95, v94
	s_waitcnt lgkmcnt(0)
	v_add_f32_e32 v94, v94, v95
	v_mov_b32_e32 v95, v94
	s_nop 1
	v_permlane16_swap_b32 v95, v94
	s_waitcnt lgkmcnt(0)
	v_add_f32_e32 v94, v94, v95
	s_nop 1
	v_mov_b32_dpp v95, v94 row_ror:8 row_mask:0xf bank_mask:0xf
	s_waitcnt lgkmcnt(0)
	v_add_f32_e32 v94, v94, v95
	s_nop 1
	v_mov_b32_dpp v95, v94 row_half_mirror row_mask:0xf bank_mask:0xf
	s_nop 1
	v_mov_b32_dpp v95, v95 quad_perm:[3,2,1,0] row_mask:0xf bank_mask:0xf
	s_waitcnt lgkmcnt(0)
	v_add_f32_e32 v94, v94, v95
	s_nop 1
	v_mov_b32_dpp v95, v94 quad_perm:[2,3,0,1] row_mask:0xf bank_mask:0xf
	s_waitcnt lgkmcnt(0)
	v_add_f32_e32 v94, v94, v95
	s_nop 1
	v_mov_b32_dpp v95, v94 quad_perm:[1,0,3,2] row_mask:0xf bank_mask:0xf
	s_waitcnt lgkmcnt(0)
	v_add_f32_e32 v94, v94, v95
	v_fmamk_f32 v94, v94, 0x3a800000, v191
	v_cmp_gt_f32_e32 vcc, s12, v94
	v_mul_f32_e32 v95, 0x4b800000, v94
	s_nop 0
	v_cndmask_b32_e32 v94, v94, v95, vcc
	v_rsq_f32_e32 v94, v94
	s_nop 0
	v_mul_f32_e32 v95, 0x45800000, v94
	v_cndmask_b32_e32 v94, v94, v95, vcc
	v_pk_mul_f32 v[0:1], v[0:1], v[94:95] op_sel_hi:[1,0]
	v_pk_mul_f32 v[2:3], v[2:3], v[94:95] op_sel_hi:[1,0]
	s_waitcnt vmcnt(0)
	v_pk_mul_f32 v[0:1], v[112:113], v[0:1]
	v_pk_mul_f32 v[2:3], v[114:115], v[2:3]
	v_cvt_pk_bf16_f32 v0, v0, v1
	v_cvt_pk_bf16_f32 v1, v2, v3
	v_pk_mul_f32 v[2:3], v[4:5], v[94:95] op_sel_hi:[1,0]
	v_pk_mul_f32 v[4:5], v[6:7], v[94:95] op_sel_hi:[1,0]
	v_pk_mul_f32 v[2:3], v[108:109], v[2:3]
	v_pk_mul_f32 v[4:5], v[110:111], v[4:5]
	v_cvt_pk_bf16_f32 v2, v2, v3
	v_cvt_pk_bf16_f32 v3, v4, v5
	v_pk_mul_f32 v[4:5], v[8:9], v[94:95] op_sel_hi:[1,0]
	v_pk_mul_f32 v[6:7], v[10:11], v[94:95] op_sel_hi:[1,0]
	v_pk_mul_f32 v[4:5], v[104:105], v[4:5]
	v_pk_mul_f32 v[6:7], v[6:7], v[106:107]
	v_cvt_pk_bf16_f32 v4, v4, v5
	v_cvt_pk_bf16_f32 v5, v6, v7
	v_pk_mul_f32 v[6:7], v[12:13], v[94:95] op_sel_hi:[1,0]
	v_pk_mul_f32 v[8:9], v[14:15], v[94:95] op_sel_hi:[1,0]
	v_pk_mul_f32 v[6:7], v[6:7], v[100:101]
	v_pk_mul_f32 v[8:9], v[8:9], v[102:103]
	v_cvt_pk_bf16_f32 v6, v6, v7
	v_cvt_pk_bf16_f32 v7, v8, v9
	global_store_dwordx4 v[74:75], v[0:3], off
	global_store_dwordx4 v[74:75], v[4:7], off offset:16
	s_nop 0
	v_mov_b32_e32 v0, v98
	s_andn2_b64 exec, exec, s[8:9]
	s_cbranch_execnz .LBB0_769
